# k3 main loop hand-rewritten: MFMA of next codebook software-pipelined into softmax VALU stream, per-row store groups, sc0sc1 stores, L2 warm-up
# baseline (speedup 1.0000x reference)
.LBB2_414:
	s_movk_i32 s0, 0xc00
	v_mov_b64_e32 v[26:27], s[42:43]
	v_mul_u32_u24_e32 v28, 0xc00, v154
	v_mad_i64_i32 v[26:27], s[0:1], v62, s0, v[26:27]
	v_or_b32_e32 v28, v28, v98
	v_mov_b32_e32 v99, 0
	v_lshl_add_u64 v[26:27], v[26:27], 0, v[98:99]
	v_or_b32_e32 v29, 0x10000, v28
	global_store_dwordx4 v[26:27], v[22:25], off
	ds_write_b128 v29, v[22:25]
	v_sub_f32_e32 v10, v10, v22
	v_or_b32_e32 v22, v101, v154
	v_sub_f32_e32 v11, v11, v23
	v_add_u32_e32 v23, v22, v102
	v_lshl_or_b32 v23, v23, 4, v103
	ds_write_b32 v23, v10
	v_add_u32_e32 v10, v22, v104
	v_lshl_or_b32 v10, v10, 4, v105
	ds_write_b32 v10, v11
	v_or_b32_e32 v10, v106, v154
	v_add_u32_e32 v10, v10, v107
	v_sub_f32_e32 v12, v12, v24
	v_lshl_or_b32 v10, v10, 4, v108
	ds_write_b32 v10, v12
	v_or_b32_e32 v10, v109, v154
	v_add_u32_e32 v10, v10, v110
	v_sub_f32_e32 v13, v13, v25
	v_lshl_or_b32 v10, v10, 4, v111
	ds_write_b32 v10, v13
	v_add_u32_e32 v10, 0x10400, v28
	ds_write_b128 v10, v[18:21]
	v_sub_f32_e32 v10, v6, v18
	v_sub_f32_e32 v11, v7, v19
	v_pk_add_f32 v[6:7], v[8:9], v[20:21] neg_lo:[0,1] neg_hi:[0,1]
	v_or_b32_e32 v8, v112, v154
	v_add_u32_e32 v9, v8, v113
	v_add_u32_e32 v8, v8, v115
	v_lshl_or_b32 v9, v9, 4, v114
	v_lshl_or_b32 v8, v8, 4, v116
	ds_write_b32 v9, v10
	ds_write_b32 v8, v11
	v_or_b32_e32 v8, v117, v154
	v_add_u32_e32 v8, v8, v118
	v_lshl_or_b32 v8, v8, 4, v119
	ds_write_b32 v8, v6
	v_or_b32_e32 v6, v120, v154
	v_add_u32_e32 v6, v6, v121
	v_lshl_or_b32 v6, v6, 4, v122
	ds_write_b32 v6, v7
	v_add_u32_e32 v6, 0x10800, v28
	ds_write_b128 v6, v[14:17]
	v_or_b32_e32 v6, v123, v154
	v_add_u32_e32 v7, v6, v124
	v_pk_add_f32 v[2:3], v[2:3], v[14:15] neg_lo:[0,1] neg_hi:[0,1]
	v_lshl_or_b32 v7, v7, 4, v125
	ds_write_b32 v7, v2
	v_add_u32_e32 v2, v6, v126
	v_lshl_or_b32 v2, v2, 4, v127
	ds_write_b32 v2, v3
	v_or_b32_e32 v2, v133, v154
	v_add_u32_e32 v2, v2, v134
	v_pk_add_f32 v[4:5], v[4:5], v[16:17] neg_lo:[0,1] neg_hi:[0,1]
	v_lshl_or_b32 v2, v2, 4, v63
	ds_write_b32 v2, v4
	v_or_b32_e32 v2, v135, v154
	v_add_u32_e32 v2, v2, v132
	v_lshl_or_b32 v2, v2, 4, v136
	v_add_lshl_u32 v4, v100, v154, 4
	s_mov_b32 s5, 0
	s_mov_b32 s4, 1.0
	ds_write_b32 v2, v5
	v_mov_b64_e32 v[2:3], s[4:5]
	v_add_u32_e32 v4, 8, v4
	s_waitcnt vmcnt(1)
	v_lshlrev_b32_e32 v40, 9, v150
	ds_write2st64_b64 v4, v[2:3], v[2:3] offset1:64
	v_or_b32_e32 v2, v40, v128
	v_lshlrev_b32_e32 v98, 4, v2
	v_lshl_add_u64 v[100:101], s[40:41], 0, v[98:99]
	s_mov_b64 s[0:1], 0x787000
	v_lshl_add_u64 v[34:35], v[100:101], 0, s[0:1]
	s_mov_b32 s0, 0x788000
	v_add_co_u32_e32 v36, vcc, s0, v100
	global_store_dwordx4 v[26:27], v[18:21], off offset:1024
	global_store_dwordx4 v[26:27], v[14:17], off offset:2048
	s_waitcnt lgkmcnt(0)
	s_barrier
	v_addc_co_u32_e32 v37, vcc, 0, v101, vcc
	s_lshr_b32 s59, s33, 4
	s_and_b32 s59, s59, 31
	s_lshl_b32 s59, s59, 15
	s_add_u32 s59, s59, 0x787000
	s_add_u32 s68, s40, s59
	s_addc_u32 s69, s41, 0
	v_lshlrev_b32_e32 v207, 6, v0
	global_load_dword v207, v207, s[68:69]
	global_load_dwordx4 v[2:5], v[34:35], off offset:1024
	global_load_dwordx4 v[10:13], v[34:35], off offset:2048
	global_load_dwordx4 v[14:17], v[34:35], off offset:3072
	global_load_dwordx4 v[6:9], v[36:37], off offset:-4096
	global_load_dwordx4 v[18:21], v[36:37], off
	global_load_dwordx4 v[22:25], v[36:37], off offset:1024
	global_load_dwordx4 v[26:29], v[36:37], off offset:2048
	global_load_dwordx4 v[30:33], v[36:37], off offset:3072
	v_and_b32_e32 v35, 15, v0
	v_lshrrev_b32_e32 v37, 4, v128
	v_lshlrev_b32_e32 v102, 2, v35
	v_lshlrev_b32_e32 v41, 2, v37
	v_lshlrev_b32_e32 v34, 4, v35
	v_cmp_gt_u32_e64 s[0:1], 6, v35
	v_mov_b32_e32 v35, v99
	v_or3_b32 v36, v34, v41, v40
	v_lshl_add_u64 v[104:105], s[44:45], 0, v[34:35]
	v_or_b32_e32 v34, v40, v34
	s_movk_i32 s4, 0x1000
	v_or3_b32 v153, v34, v41, s4
	v_or_b32_e32 v34, 0x11800, v98
	v_lshl_add_u64 v[118:119], s[40:41], 0, v[34:35]
	v_or_b32_e32 v34, 0x11400, v98
	v_lshl_add_u64 v[120:121], s[40:41], 0, v[34:35]
	v_or_b32_e32 v34, 0x11000, v98
	ds_read2st64_b32 v[132:133], v36 offset1:1
	v_or_b32_e32 v36, s33, v41
	v_lshl_add_u64 v[122:123], s[40:41], 0, v[34:35]
	v_or_b32_e32 v34, 0x10c00, v98
	v_or_b32_e32 v38, 1, v36
	v_lshl_add_u64 v[124:125], s[40:41], 0, v[34:35]
	v_or_b32_e32 v34, 0x10800, v98
	v_mul_u32_u24_e32 v152, 0x3000, v37
	v_ashrrev_i32_e32 v37, 31, v36
	v_ashrrev_i32_e32 v39, 31, v38
	v_lshl_add_u64 v[126:127], s[40:41], 0, v[34:35]
	v_or_b32_e32 v34, 0x10400, v98
	v_mov_b32_e32 v103, v99
	v_lshlrev_b64 v[108:109], 17, v[36:37]
	v_lshlrev_b64 v[110:111], 17, v[38:39]
	v_or_b32_e32 v38, 2, v36
	v_or_b32_e32 v36, 3, v36
	v_lshl_add_u64 v[128:129], s[40:41], 0, v[34:35]
	v_mul_u32_u24_e32 v34, 24, v150
	v_lshl_add_u64 v[106:107], s[38:39], 0, v[102:103]
	v_ashrrev_i32_e32 v39, 31, v38
	v_ashrrev_i32_e32 v37, 31, v36
	v_lshlrev_b32_e32 v103, 2, v0
	v_or_b32_e32 v98, 0x11c00, v98
	v_or_b32_e32 v34, v152, v34
	v_lshlrev_b64 v[112:113], 17, v[38:39]
	v_lshlrev_b64 v[114:115], 17, v[36:37]
	v_and_b32_e32 v116, 0x700, v103
	v_mov_b32_e32 v117, v99
	v_lshl_add_u64 v[130:131], s[40:41], 0, v[98:99]
	v_add_u32_e32 v154, v34, v102
	s_mov_b64 s[6:7], 0
	s_mov_b64 s[8:9], 0x800
	v_mov_b32_e32 v155, 0x400
	v_mov_b32_e32 v159, 0
	v_mov_b32_e32 v158, 0
	v_mov_b32_e32 v157, 0
	v_mov_b32_e32 v156, 0
	v_readfirstlane_b32 s78, v150
	v_and_b32_e32 v104, 63, v0
	v_lshlrev_b32_e32 v104, 4, v104
	v_lshl_or_b32 v104, v150, 13, v104
	v_add_u32_e32 v105, 0xfffff000, v153
	v_mov_b32_e32 v106, v154
	v_lshrrev_b32_e32 v98, 2, v102
	v_cmp_gt_u32_e32 vcc, 6, v98
	v_add_u32_e32 v107, -6, v98
	s_nop 0
	v_cndmask_b32_e32 v107, v107, v98, vcc
	v_cmp_gt_u32_e32 vcc, 6, v107
	v_add_u32_e32 v98, -6, v107
	s_nop 0
	v_cndmask_b32_e32 v107, v98, v107, vcc
	v_lshlrev_b32_e32 v107, 2, v107
	v_sub_u32_e32 v106, v106, v102
	v_add_u32_e32 v106, v106, v107
	v_and_b32_e32 v98, 63, v0
	v_lshrrev_b32_e32 v98, 4, v98
	v_lshlrev_b32_e32 v98, 19, v98
	v_lshl_or_b32 v108, v102, 2, v98
	v_add_u32_e32 v109, 0x20000, v108
	v_add_u32_e32 v110, 0x40000, v108
	v_add_u32_e32 v111, 0x60000, v108
	v_mov_b32_e32 v240, 0
	v_mov_b32_e32 v241, 0
	v_mov_b32_e32 v242, 0
	v_mov_b32_e32 v243, 0
	s_lshl_b32 s84, s33, 17
	s_lshl_b32 s85, s78, 10
	s_add_u32 s84, s84, s85
	s_add_u32 s80, s44, s84
	s_addc_u32 s81, s45, 0
	s_mul_i32 s84, s78, 0x1800
	s_add_u32 s94, s38, s84
	s_addc_u32 s95, s39, 0
	s_mov_b32 s70, 0
	s_add_u32 s86, s40, 0x797000
	s_addc_u32 s87, s41, 0
	s_add_u32 s88, s86, 0x1000
	s_addc_u32 s89, s87, 0
	v_add_u32_e32 v112, 0x1000, v105
	s_waitcnt vmcnt(0) lgkmcnt(0)
	v_mfma_f32_16x16x4_f32 v[34:37], v132, v6, 0
	v_mfma_f32_16x16x4_f32 v[38:41], v132, v8, 0
	v_mfma_f32_16x16x4_f32 v[34:37], v133, v7, v[34:37]
	v_mfma_f32_16x16x4_f32 v[38:41], v133, v9, v[38:41]
	global_load_dwordx4 v[6:9], v104, s[86:87]
	v_mfma_f32_16x16x4_f32 v[42:45], v132, v2, 0
	v_mfma_f32_16x16x4_f32 v[46:49], v132, v4, 0
	v_mfma_f32_16x16x4_f32 v[42:45], v133, v3, v[42:45]
	v_mfma_f32_16x16x4_f32 v[46:49], v133, v5, v[46:49]
	global_load_dwordx4 v[2:5], v104, s[86:87] offset:1024
	v_mfma_f32_16x16x4_f32 v[50:53], v132, v10, 0
	v_mfma_f32_16x16x4_f32 v[54:57], v132, v12, 0
	v_mfma_f32_16x16x4_f32 v[50:53], v133, v11, v[50:53]
	v_mfma_f32_16x16x4_f32 v[54:57], v133, v13, v[54:57]
	global_load_dwordx4 v[10:13], v104, s[86:87] offset:2048
	v_mfma_f32_16x16x4_f32 v[58:61], v132, v14, 0
	v_mfma_f32_16x16x4_f32 v[62:65], v132, v16, 0
	v_mfma_f32_16x16x4_f32 v[58:61], v133, v15, v[58:61]
	v_mfma_f32_16x16x4_f32 v[62:65], v133, v17, v[62:65]
	global_load_dwordx4 v[14:17], v104, s[86:87] offset:3072
	v_mfma_f32_16x16x4_f32 v[66:69], v132, v18, 0
	v_mfma_f32_16x16x4_f32 v[70:73], v132, v20, 0
	v_mfma_f32_16x16x4_f32 v[66:69], v133, v19, v[66:69]
	v_mfma_f32_16x16x4_f32 v[70:73], v133, v21, v[70:73]
	global_load_dwordx4 v[18:21], v104, s[88:89]
	v_mfma_f32_16x16x4_f32 v[74:77], v132, v22, 0
	v_mfma_f32_16x16x4_f32 v[78:81], v132, v24, 0
	v_mfma_f32_16x16x4_f32 v[74:77], v133, v23, v[74:77]
	v_mfma_f32_16x16x4_f32 v[78:81], v133, v25, v[78:81]
	global_load_dwordx4 v[22:25], v104, s[88:89] offset:1024
	v_mfma_f32_16x16x4_f32 v[82:85], v132, v26, 0
	v_mfma_f32_16x16x4_f32 v[86:89], v132, v28, 0
	v_mfma_f32_16x16x4_f32 v[82:85], v133, v27, v[82:85]
	v_mfma_f32_16x16x4_f32 v[86:89], v133, v29, v[86:89]
	global_load_dwordx4 v[26:29], v104, s[88:89] offset:2048
	v_mfma_f32_16x16x4_f32 v[90:93], v132, v30, 0
	v_mfma_f32_16x16x4_f32 v[94:97], v132, v32, 0
	v_mfma_f32_16x16x4_f32 v[90:93], v133, v31, v[90:93]
	v_mfma_f32_16x16x4_f32 v[94:97], v133, v33, v[94:97]
	global_load_dwordx4 v[30:33], v104, s[88:89] offset:3072
	ds_read2st64_b32 v[132:133], v112 offset1:1
	s_nop 7
	s_nop 7
	v_max3_f32 v114, v34, v38, v42
	v_max3_f32 v116, v46, v50, v54
	v_max3_f32 v114, v114, v58, v62
	v_max3_f32 v116, v116, v66, v70
	v_max3_f32 v114, v114, v74, v78
	v_max3_f32 v116, v116, v82, v86
	v_max3_f32 v114, v114, v90, v94
	v_max_f32_e32 v114, v114, v116
	s_nop 1
	v_max_f32_dpp v114, v114, v114 row_ror:1 row_mask:0xf bank_mask:0xf
	s_nop 1
	v_max_f32_dpp v114, v114, v114 row_ror:2 row_mask:0xf bank_mask:0xf
	s_nop 1
	v_max_f32_dpp v114, v114, v114 row_ror:4 row_mask:0xf bank_mask:0xf
	s_nop 1
	v_max_f32_dpp v114, v114, v114 row_ror:8 row_mask:0xf bank_mask:0xf
	s_waitcnt vmcnt(0) lgkmcnt(0)
.Lk3m_loop:
	s_waitcnt lgkmcnt(0)
	s_lshl_b32 s84, s70, 13
	s_add_u32 s90, s80, s84
	s_addc_u32 s91, s81, 0
	s_mul_i32 s84, s70, 0xc000
	s_add_u32 s92, s94, s84
	s_addc_u32 s93, s95, 0
	s_add_i32 s84, s70, 2
	s_and_b32 s84, s84, 15
	s_lshl_b32 s82, s84, 12
	s_lshl_b32 s84, s84, 16
	s_add_u32 s84, s84, 0x787000
	s_add_u32 s86, s40, s84
	s_addc_u32 s87, s41, 0
	s_add_u32 s88, s86, 0x1000
	s_addc_u32 s89, s87, 0
	s_add_i32 s84, s70, 15
	s_and_b32 s84, s84, 15
	s_mul_i32 s84, s84, 0xc0
	s_add_u32 s83, s84, 0x10000
	v_add_u32_e32 v112, s82, v105
	v_sub_f32_e32 v120, v94, v114
	v_cmp_eq_f32_e64 s[72:73], v94, v114
	s_waitcnt vmcnt(27)
	v_mfma_f32_16x16x4_f32 v[176:179], v132, v6, 0
	ds_read2st64_b32 v[254:255], v112 offset1:1
	v_sub_f32_e32 v121, v90, v114
	v_cmp_eq_f32_e64 s[74:75], v90, v114
	v_exp_f32_e32 v149, v120
	v_cndmask_b32_e64 v118, v155, 15, s[72:73]
	v_max3_f32 v115, v35, v39, v43
	v_sub_f32_e32 v120, v86, v114
	v_cmp_eq_f32_e64 s[76:77], v86, v114
	v_exp_f32_e32 v148, v121
	v_cndmask_b32_e64 v118, v118, 14, s[74:75]
	v_mfma_f32_16x16x4_f32 v[180:183], v132, v8, 0
	v_sub_f32_e32 v121, v82, v114
	v_max3_f32 v117, v47, v51, v55
	v_cmp_eq_f32_e64 s[72:73], v82, v114
	v_exp_f32_e32 v147, v120
	v_cndmask_b32_e64 v118, v118, 13, s[76:77]
	v_sub_f32_e32 v120, v78, v114
	v_cmp_eq_f32_e64 s[74:75], v78, v114
	v_max3_f32 v115, v115, v59, v63
	v_exp_f32_e32 v146, v121
	v_cndmask_b32_e64 v118, v118, 12, s[72:73]
	v_mfma_f32_16x16x4_f32 v[176:179], v133, v7, v[176:179]
	v_sub_f32_e32 v121, v74, v114
	v_cmp_eq_f32_e64 s[76:77], v74, v114
	v_exp_f32_e32 v145, v120
	v_cndmask_b32_e64 v118, v118, 11, s[74:75]
	v_max3_f32 v117, v117, v67, v71
	v_sub_f32_e32 v120, v70, v114
	v_cmp_eq_f32_e64 s[72:73], v70, v114
	v_exp_f32_e32 v144, v121
	v_cndmask_b32_e64 v118, v118, 10, s[76:77]
	v_mfma_f32_16x16x4_f32 v[180:183], v133, v9, v[180:183]
	global_load_dwordx4 v[6:9], v104, s[86:87]
	v_sub_f32_e32 v121, v66, v114
	v_max3_f32 v115, v115, v75, v79
	v_cmp_eq_f32_e64 s[74:75], v66, v114
	v_exp_f32_e32 v143, v120
	v_cndmask_b32_e64 v118, v118, 9, s[72:73]
	v_sub_f32_e32 v120, v62, v114
	v_cmp_eq_f32_e64 s[76:77], v62, v114
	v_max3_f32 v117, v117, v83, v87
	v_exp_f32_e32 v142, v121
	v_cndmask_b32_e64 v118, v118, 8, s[74:75]
	s_waitcnt vmcnt(27)
	v_mfma_f32_16x16x4_f32 v[184:187], v132, v2, 0
	v_sub_f32_e32 v121, v58, v114
	v_cmp_eq_f32_e64 s[72:73], v58, v114
	v_exp_f32_e32 v141, v120
	v_cndmask_b32_e64 v118, v118, 7, s[76:77]
	v_max3_f32 v115, v115, v91, v95
	v_sub_f32_e32 v120, v54, v114
	v_cmp_eq_f32_e64 s[74:75], v54, v114
	v_exp_f32_e32 v140, v121
	v_cndmask_b32_e64 v118, v118, 6, s[72:73]
	v_mfma_f32_16x16x4_f32 v[188:191], v132, v4, 0
	v_sub_f32_e32 v121, v50, v114
	v_max_f32_e32 v115, v115, v117
	v_cmp_eq_f32_e64 s[76:77], v50, v114
	v_exp_f32_e32 v139, v120
	v_cndmask_b32_e64 v118, v118, 5, s[74:75]
	v_sub_f32_e32 v120, v46, v114
	v_cmp_eq_f32_e64 s[72:73], v46, v114
	v_max_f32_dpp v115, v115, v115 row_ror:1 row_mask:0xf bank_mask:0xf
	v_exp_f32_e32 v138, v121
	v_cndmask_b32_e64 v118, v118, 4, s[76:77]
	v_mfma_f32_16x16x4_f32 v[184:187], v133, v3, v[184:187]
	v_sub_f32_e32 v121, v42, v114
	v_cmp_eq_f32_e64 s[74:75], v42, v114
	v_exp_f32_e32 v137, v120
	v_cndmask_b32_e64 v118, v118, 3, s[72:73]
	v_max_f32_dpp v115, v115, v115 row_ror:2 row_mask:0xf bank_mask:0xf
	v_sub_f32_e32 v120, v38, v114
	v_cmp_eq_f32_e64 s[76:77], v38, v114
	v_exp_f32_e32 v136, v121
	v_cndmask_b32_e64 v118, v118, 2, s[74:75]
	v_mfma_f32_16x16x4_f32 v[188:191], v133, v5, v[188:191]
	global_load_dwordx4 v[2:5], v104, s[86:87] offset:1024
	v_sub_f32_e32 v121, v34, v114
	v_max_f32_dpp v115, v115, v115 row_ror:4 row_mask:0xf bank_mask:0xf
	v_cmp_eq_f32_e64 s[72:73], v34, v114
	v_exp_f32_e32 v135, v120
	v_cndmask_b32_e64 v118, v118, 1, s[76:77]
	v_exp_f32_e32 v134, v121
	v_cndmask_b32_e64 v118, v118, 0, s[72:73]
	v_max_f32_dpp v115, v115, v115 row_ror:8 row_mask:0xf bank_mask:0xf
	v_sub_f32_e32 v120, v95, v115
	v_cmp_eq_f32_e64 s[72:73], v95, v115
	v_max3_f32 v114, v36, v40, v44
	s_waitcnt vmcnt(27)
	v_mfma_f32_16x16x4_f32 v[192:195], v132, v10, 0
	v_sub_f32_e32 v121, v91, v115
	v_and_b32_e32 v122, 12, v118
	v_cmp_eq_f32_e64 s[74:75], v91, v115
	v_and_b32_e32 v124, 3, v118
	v_exp_f32_e32 v175, v120
	v_add_f32_e32 v128, v134, v135
	v_cndmask_b32_e64 v119, v155, 15, s[72:73]
	v_add_f32_e32 v130, v136, v137
	v_sub_f32_e32 v120, v87, v115
	v_max3_f32 v116, v48, v52, v56
	v_cmp_eq_f32_e64 s[76:77], v87, v115
	v_exp_f32_e32 v174, v121
	v_lshl_or_b32 v122, v122, 4, v124
	v_cndmask_b32_e64 v119, v119, 14, s[74:75]
	v_add_f32_e32 v128, v128, v138
	v_mfma_f32_16x16x4_f32 v[196:199], v132, v12, 0
	v_sub_f32_e32 v121, v83, v115
	v_add_f32_e32 v130, v130, v139
	v_cmp_eq_f32_e64 s[72:73], v83, v115
	v_or_b32_e32 v122, v122, v102
	v_exp_f32_e32 v173, v120
	v_max3_f32 v114, v114, v60, v64
	v_cndmask_b32_e64 v119, v119, 13, s[76:77]
	v_add_f32_e32 v128, v128, v140
	v_sub_f32_e32 v120, v79, v115
	v_cmp_eq_f32_e64 s[74:75], v79, v115
	v_add_f32_e32 v130, v130, v141
	v_exp_f32_e32 v172, v121
	v_max_u32_e32 v126, v122, v118
	v_cndmask_b32_e64 v119, v119, 12, s[72:73]
	v_max3_f32 v116, v116, v68, v72
	v_mfma_f32_16x16x4_f32 v[192:195], v133, v11, v[192:195]
	v_sub_f32_e32 v121, v75, v115
	v_add_f32_e32 v128, v128, v142
	v_cmp_eq_f32_e64 s[76:77], v75, v115
	v_add_f32_e32 v130, v130, v143
	v_exp_f32_e32 v171, v120
	v_min_u32_dpp v126, v126, v126 row_ror:1 row_mask:0xf bank_mask:0xf
	v_cndmask_b32_e64 v119, v119, 11, s[74:75]
	v_sub_f32_e32 v120, v71, v115
	v_add_f32_e32 v128, v128, v144
	v_cmp_eq_f32_e64 s[72:73], v71, v115
	v_max3_f32 v114, v114, v76, v80
	v_exp_f32_e32 v170, v121
	v_add_f32_e32 v130, v130, v145
	v_cndmask_b32_e64 v119, v119, 10, s[76:77]
	v_min_u32_dpp v126, v126, v126 row_ror:2 row_mask:0xf bank_mask:0xf
	v_mfma_f32_16x16x4_f32 v[196:199], v133, v13, v[196:199]
	global_load_dwordx4 v[10:13], v104, s[86:87] offset:2048
	v_sub_f32_e32 v121, v67, v115
	v_add_f32_e32 v128, v128, v146
	v_cmp_eq_f32_e64 s[74:75], v67, v115
	v_max3_f32 v116, v116, v84, v88
	v_exp_f32_e32 v169, v120
	v_cndmask_b32_e64 v119, v119, 9, s[72:73]
	v_add_f32_e32 v130, v130, v147
	v_sub_f32_e32 v120, v63, v115
	v_min_u32_dpp v126, v126, v126 row_ror:4 row_mask:0xf bank_mask:0xf
	v_cmp_eq_f32_e64 s[76:77], v63, v115
	v_add_f32_e32 v128, v128, v148
	v_exp_f32_e32 v168, v121
	v_add_f32_e32 v130, v130, v149
	v_cndmask_b32_e64 v119, v119, 8, s[74:75]
	v_max3_f32 v114, v114, v92, v96
	s_waitcnt vmcnt(24)
	v_mfma_f32_16x16x4_f32 v[200:203], v132, v14, 0
	v_sub_f32_e32 v121, v59, v115
	v_min_u32_dpp v126, v126, v126 row_ror:8 row_mask:0xf bank_mask:0xf
	v_cmp_eq_f32_e64 s[72:73], v59, v115
	v_exp_f32_e32 v167, v120
	v_add_f32_e32 v128, v128, v130
	v_cndmask_b32_e64 v119, v119, 7, s[76:77]
	v_mad_u32_u24 v248, v126, 24, v107
	v_sub_f32_e32 v120, v55, v115
	v_add_f32_dpp v128, v128, v128 row_ror:1 row_mask:0xf bank_mask:0xf
	v_cmp_eq_f32_e64 s[74:75], v55, v115
	v_max_f32_e32 v114, v114, v116
	v_exp_f32_e32 v166, v121
	global_load_dword v240, v248, s[92:93]
	v_cndmask_b32_e64 v119, v119, 6, s[72:73]
	v_add_f32_dpp v128, v128, v128 row_ror:2 row_mask:0xf bank_mask:0xf
	v_mfma_f32_16x16x4_f32 v[204:207], v132, v16, 0
	v_sub_f32_e32 v121, v51, v115
	v_cmp_eq_f32_e64 s[76:77], v51, v115
	v_add_f32_dpp v128, v128, v128 row_ror:4 row_mask:0xf bank_mask:0xf
	v_exp_f32_e32 v165, v120
	v_max_f32_dpp v114, v114, v114 row_ror:1 row_mask:0xf bank_mask:0xf
	v_cndmask_b32_e64 v119, v119, 5, s[74:75]
	v_add_f32_dpp v128, v128, v128 row_ror:8 row_mask:0xf bank_mask:0xf
	v_sub_f32_e32 v120, v47, v115
	v_rcp_f32_e32 v244, v128
	v_cmp_eq_f32_e64 s[72:73], v47, v115
	v_pk_mul_f32 v[134:135], v[244:245], v[134:135] op_sel_hi:[0,1]
	v_exp_f32_e32 v164, v121
	v_pk_mul_f32 v[136:137], v[244:245], v[136:137] op_sel_hi:[0,1]
	v_cndmask_b32_e64 v119, v119, 4, s[76:77]
	v_mfma_f32_16x16x4_f32 v[200:203], v133, v15, v[200:203]
	v_sub_f32_e32 v121, v43, v115
	v_max_f32_dpp v114, v114, v114 row_ror:2 row_mask:0xf bank_mask:0xf
	v_cmp_eq_f32_e64 s[74:75], v43, v115
	global_store_dwordx4 v108, v[134:137], s[90:91] sc0 sc1
	v_exp_f32_e32 v163, v120
	v_pk_mul_f32 v[138:139], v[244:245], v[138:139] op_sel_hi:[0,1]
	v_cndmask_b32_e64 v119, v119, 3, s[72:73]
	v_pk_mul_f32 v[140:141], v[244:245], v[140:141] op_sel_hi:[0,1]
	v_sub_f32_e32 v120, v39, v115
	v_max_f32_dpp v114, v114, v114 row_ror:4 row_mask:0xf bank_mask:0xf
	v_cmp_eq_f32_e64 s[76:77], v39, v115
	global_store_dwordx4 v108, v[138:141], s[90:91] offset:256 sc0 sc1
	v_exp_f32_e32 v162, v121
	v_cndmask_b32_e64 v119, v119, 2, s[74:75]
	v_pk_mul_f32 v[142:143], v[244:245], v[142:143] op_sel_hi:[0,1]
	v_mfma_f32_16x16x4_f32 v[204:207], v133, v17, v[204:207]
	global_load_dwordx4 v[14:17], v104, s[86:87] offset:3072
	v_sub_f32_e32 v121, v35, v115
	v_pk_mul_f32 v[144:145], v[244:245], v[144:145] op_sel_hi:[0,1]
	v_cmp_eq_f32_e64 s[72:73], v35, v115
	global_store_dwordx4 v108, v[142:145], s[90:91] offset:512 sc0 sc1
	v_exp_f32_e32 v161, v120
	v_max_f32_dpp v114, v114, v114 row_ror:8 row_mask:0xf bank_mask:0xf
	v_cndmask_b32_e64 v119, v119, 1, s[76:77]
	v_pk_mul_f32 v[146:147], v[244:245], v[146:147] op_sel_hi:[0,1]
	v_exp_f32_e32 v160, v121
	v_pk_mul_f32 v[148:149], v[244:245], v[148:149] op_sel_hi:[0,1]
	v_cndmask_b32_e64 v119, v119, 0, s[72:73]
	global_store_dwordx4 v108, v[146:149], s[90:91] offset:768 sc0 sc1
	v_sub_f32_e32 v120, v96, v114
	v_cmp_eq_f32_e64 s[72:73], v96, v114
	s_waitcnt vmcnt(13)
	s_waitcnt vmcnt(27)
	v_mfma_f32_16x16x4_f32 v[208:211], v132, v18, 0
	v_sub_f32_e32 v121, v92, v114
	v_add_u32_e32 v113, s83, v106
	v_cmp_eq_f32_e64 s[74:75], v92, v114
	ds_read2st64_b32 v[250:251], v113 offset1:12
	v_exp_f32_e32 v149, v120
	ds_read2st64_b32 v[252:253], v113 offset0:24 offset1:36
	v_cndmask_b32_e64 v118, v155, 15, s[72:73]
	v_max3_f32 v115, v37, v41, v45
	v_sub_f32_e32 v120, v88, v114
	v_and_b32_e32 v123, 12, v119
	v_cmp_eq_f32_e64 s[76:77], v88, v114
	v_and_b32_e32 v125, 3, v119
	v_exp_f32_e32 v148, v121
	v_add_f32_e32 v129, v160, v161
	v_cndmask_b32_e64 v118, v118, 14, s[74:75]
	v_add_f32_e32 v131, v162, v163
	v_mfma_f32_16x16x4_f32 v[212:215], v132, v20, 0
	v_sub_f32_e32 v121, v84, v114
	v_max3_f32 v117, v49, v53, v57
	v_cmp_eq_f32_e64 s[72:73], v84, v114
	v_lshl_or_b32 v123, v123, 4, v125
	v_exp_f32_e32 v147, v120
	v_cndmask_b32_e64 v118, v118, 13, s[76:77]
	v_add_f32_e32 v129, v129, v164
	v_sub_f32_e32 v120, v80, v114
	v_add_f32_e32 v131, v131, v165
	v_cmp_eq_f32_e64 s[74:75], v80, v114
	v_or_b32_e32 v123, v123, v102
	v_exp_f32_e32 v146, v121
	v_max3_f32 v115, v115, v61, v65
	v_cndmask_b32_e64 v118, v118, 12, s[72:73]
	v_add_f32_e32 v129, v129, v166
	v_mfma_f32_16x16x4_f32 v[208:211], v133, v19, v[208:211]
	v_sub_f32_e32 v121, v76, v114
	v_add_f32_e32 v131, v131, v167
	v_cmp_eq_f32_e64 s[76:77], v76, v114
	v_max_u32_e32 v127, v123, v119
	v_exp_f32_e32 v145, v120
	v_max3_f32 v117, v117, v69, v73
	v_cndmask_b32_e64 v118, v118, 11, s[74:75]
	v_add_f32_e32 v129, v129, v168
	v_sub_f32_e32 v120, v72, v114
	v_add_f32_e32 v131, v131, v169
	v_cmp_eq_f32_e64 s[72:73], v72, v114
	v_min_u32_dpp v127, v127, v127 row_ror:1 row_mask:0xf bank_mask:0xf
	v_exp_f32_e32 v144, v121
	v_add_f32_e32 v129, v129, v170
	v_cndmask_b32_e64 v118, v118, 10, s[76:77]
	v_mfma_f32_16x16x4_f32 v[212:215], v133, v21, v[212:215]
	global_load_dwordx4 v[18:21], v104, s[88:89]
	v_sub_f32_e32 v121, v68, v114
	v_max3_f32 v115, v115, v77, v81
	v_cmp_eq_f32_e64 s[74:75], v68, v114
	v_add_f32_e32 v131, v131, v171
	v_exp_f32_e32 v143, v120
	v_min_u32_dpp v127, v127, v127 row_ror:2 row_mask:0xf bank_mask:0xf
	v_cndmask_b32_e64 v118, v118, 9, s[72:73]
	v_add_f32_e32 v129, v129, v172
	v_sub_f32_e32 v120, v64, v114
	v_max3_f32 v117, v117, v85, v89
	v_cmp_eq_f32_e64 s[76:77], v64, v114
	v_add_f32_e32 v131, v131, v173
	v_exp_f32_e32 v142, v121
	v_min_u32_dpp v127, v127, v127 row_ror:4 row_mask:0xf bank_mask:0xf
	v_cndmask_b32_e64 v118, v118, 8, s[74:75]
	v_add_f32_e32 v129, v129, v174
	s_waitcnt vmcnt(24)
	v_mfma_f32_16x16x4_f32 v[216:219], v132, v22, 0
	v_sub_f32_e32 v121, v60, v114
	v_add_f32_e32 v131, v131, v175
	v_cmp_eq_f32_e64 s[72:73], v60, v114
	v_max3_f32 v115, v115, v93, v97
	v_exp_f32_e32 v141, v120
	v_min_u32_dpp v127, v127, v127 row_ror:8 row_mask:0xf bank_mask:0xf
	v_cndmask_b32_e64 v118, v118, 7, s[76:77]
	v_add_f32_e32 v129, v129, v131
	v_sub_f32_e32 v120, v56, v114
	v_cmp_eq_f32_e64 s[74:75], v56, v114
	v_mad_u32_u24 v249, v127, 24, v107
	v_exp_f32_e32 v140, v121
	v_add_f32_dpp v129, v129, v129 row_ror:1 row_mask:0xf bank_mask:0xf
	v_cndmask_b32_e64 v118, v118, 6, s[72:73]
	v_max_f32_e32 v115, v115, v117
	v_mfma_f32_16x16x4_f32 v[220:223], v132, v24, 0
	v_sub_f32_e32 v121, v52, v114
	global_load_dword v241, v249, s[92:93]
	v_cmp_eq_f32_e64 s[76:77], v52, v114
	v_add_f32_dpp v129, v129, v129 row_ror:2 row_mask:0xf bank_mask:0xf
	v_exp_f32_e32 v139, v120
	s_nop 0
	v_add_f32_dpp v129, v129, v129 row_ror:4 row_mask:0xf bank_mask:0xf
	v_cndmask_b32_e64 v118, v118, 5, s[74:75]
	v_max_f32_dpp v115, v115, v115 row_ror:1 row_mask:0xf bank_mask:0xf
	v_sub_f32_e32 v120, v48, v114
	v_add_f32_dpp v129, v129, v129 row_ror:8 row_mask:0xf bank_mask:0xf
	v_cmp_eq_f32_e64 s[72:73], v48, v114
	v_rcp_f32_e32 v246, v129
	v_exp_f32_e32 v138, v121
	v_pk_mul_f32 v[160:161], v[246:247], v[160:161] op_sel_hi:[0,1]
	v_cndmask_b32_e64 v118, v118, 4, s[76:77]
	v_pk_mul_f32 v[162:163], v[246:247], v[162:163] op_sel_hi:[0,1]
	v_mfma_f32_16x16x4_f32 v[216:219], v133, v23, v[216:219]
	v_sub_f32_e32 v121, v44, v114
	v_max_f32_dpp v115, v115, v115 row_ror:2 row_mask:0xf bank_mask:0xf
	v_cmp_eq_f32_e64 s[74:75], v44, v114
	v_exp_f32_e32 v137, v120
	global_store_dwordx4 v109, v[160:163], s[90:91] sc0 sc1
	v_cndmask_b32_e64 v118, v118, 3, s[72:73]
	v_pk_mul_f32 v[164:165], v[246:247], v[164:165] op_sel_hi:[0,1]
	v_sub_f32_e32 v120, v40, v114
	v_pk_mul_f32 v[166:167], v[246:247], v[166:167] op_sel_hi:[0,1]
	v_cmp_eq_f32_e64 s[76:77], v40, v114
	v_max_f32_dpp v115, v115, v115 row_ror:4 row_mask:0xf bank_mask:0xf
	v_exp_f32_e32 v136, v121
	global_store_dwordx4 v109, v[164:167], s[90:91] offset:256 sc0 sc1
	v_cndmask_b32_e64 v118, v118, 2, s[74:75]
	v_pk_mul_f32 v[168:169], v[246:247], v[168:169] op_sel_hi:[0,1]
	v_mfma_f32_16x16x4_f32 v[220:223], v133, v25, v[220:223]
	global_load_dwordx4 v[22:25], v104, s[88:89] offset:1024
	v_sub_f32_e32 v121, v36, v114
	v_pk_mul_f32 v[170:171], v[246:247], v[170:171] op_sel_hi:[0,1]
	v_cmp_eq_f32_e64 s[72:73], v36, v114
	global_store_dwordx4 v109, v[168:171], s[90:91] offset:512 sc0 sc1
	v_exp_f32_e32 v135, v120
	v_max_f32_dpp v115, v115, v115 row_ror:8 row_mask:0xf bank_mask:0xf
	v_cndmask_b32_e64 v118, v118, 1, s[76:77]
	v_pk_mul_f32 v[172:173], v[246:247], v[172:173] op_sel_hi:[0,1]
	v_exp_f32_e32 v134, v121
	v_pk_mul_f32 v[174:175], v[246:247], v[174:175] op_sel_hi:[0,1]
	v_cndmask_b32_e64 v118, v118, 0, s[72:73]
	global_store_dwordx4 v109, v[172:175], s[90:91] offset:768 sc0 sc1
	v_sub_f32_e32 v120, v97, v115
	v_cmp_eq_f32_e64 s[72:73], v97, v115
	s_waitcnt lgkmcnt(0)
	s_waitcnt vmcnt(27)
	v_mfma_f32_16x16x4_f32 v[224:227], v132, v26, 0
	v_sub_f32_e32 v121, v93, v115
	v_add_f32_e32 v250, v159, v250
	v_cmp_eq_f32_e64 s[74:75], v93, v115
	v_add_f32_e32 v251, v158, v251
	v_exp_f32_e32 v175, v120
	v_cndmask_b32_e64 v119, v155, 15, s[72:73]
	v_add_f32_e32 v252, v157, v252
	v_sub_f32_e32 v120, v89, v115
	v_add_f32_e32 v253, v156, v253
	v_cmp_eq_f32_e64 s[76:77], v89, v115
	ds_write2st64_b32 v113, v250, v251 offset1:12
	v_exp_f32_e32 v174, v121
	ds_write2st64_b32 v113, v252, v253 offset0:24 offset1:36
	v_cndmask_b32_e64 v119, v119, 14, s[74:75]
	v_mfma_f32_16x16x4_f32 v[228:231], v132, v28, 0
	v_sub_f32_e32 v121, v85, v115
	v_and_b32_e32 v122, 12, v118
	v_cmp_eq_f32_e64 s[72:73], v85, v115
	v_and_b32_e32 v124, 3, v118
	v_exp_f32_e32 v173, v120
	v_add_f32_e32 v128, v134, v135
	v_cndmask_b32_e64 v119, v119, 13, s[76:77]
	v_sub_f32_e32 v120, v81, v115
	v_add_f32_e32 v130, v136, v137
	v_cmp_eq_f32_e64 s[74:75], v81, v115
	v_lshl_or_b32 v122, v122, 4, v124
	v_exp_f32_e32 v172, v121
	v_add_f32_e32 v128, v128, v138
	v_cndmask_b32_e64 v119, v119, 12, s[72:73]
	v_add_f32_e32 v130, v130, v139
	v_mfma_f32_16x16x4_f32 v[224:227], v133, v27, v[224:227]
	v_sub_f32_e32 v121, v77, v115
	v_cmp_eq_f32_e64 s[76:77], v77, v115
	v_or_b32_e32 v122, v122, v102
	v_exp_f32_e32 v171, v120
	v_add_f32_e32 v128, v128, v140
	v_cndmask_b32_e64 v119, v119, 11, s[74:75]
	v_add_f32_e32 v130, v130, v141
	v_sub_f32_e32 v120, v73, v115
	v_cmp_eq_f32_e64 s[72:73], v73, v115
	v_max_u32_e32 v126, v122, v118
	v_exp_f32_e32 v170, v121
	v_add_f32_e32 v128, v128, v142
	v_cndmask_b32_e64 v119, v119, 10, s[76:77]
	v_add_f32_e32 v130, v130, v143
	v_mfma_f32_16x16x4_f32 v[228:231], v133, v29, v[228:231]
	global_load_dwordx4 v[26:29], v104, s[88:89] offset:2048
	v_sub_f32_e32 v121, v69, v115
	v_min_u32_dpp v126, v126, v126 row_ror:1 row_mask:0xf bank_mask:0xf
	v_cmp_eq_f32_e64 s[74:75], v69, v115
	v_exp_f32_e32 v169, v120
	v_add_f32_e32 v128, v128, v144
	v_cndmask_b32_e64 v119, v119, 9, s[72:73]
	v_add_f32_e32 v130, v130, v145
	v_sub_f32_e32 v120, v65, v115
	v_min_u32_dpp v126, v126, v126 row_ror:2 row_mask:0xf bank_mask:0xf
	v_cmp_eq_f32_e64 s[76:77], v65, v115
	v_add_f32_e32 v128, v128, v146
	v_exp_f32_e32 v168, v121
	v_cndmask_b32_e64 v119, v119, 8, s[74:75]
	v_add_f32_e32 v130, v130, v147
	s_waitcnt vmcnt(24)
	v_mfma_f32_16x16x4_f32 v[232:235], v132, v30, 0
	v_sub_f32_e32 v121, v61, v115
	v_min_u32_dpp v126, v126, v126 row_ror:4 row_mask:0xf bank_mask:0xf
	v_cmp_eq_f32_e64 s[72:73], v61, v115
	v_add_f32_e32 v128, v128, v148
	v_exp_f32_e32 v167, v120
	v_cndmask_b32_e64 v119, v119, 7, s[76:77]
	v_add_f32_e32 v130, v130, v149
	v_sub_f32_e32 v120, v57, v115
	v_min_u32_dpp v126, v126, v126 row_ror:8 row_mask:0xf bank_mask:0xf
	v_cmp_eq_f32_e64 s[74:75], v57, v115
	v_add_f32_e32 v128, v128, v130
	v_exp_f32_e32 v166, v121
	v_mad_u32_u24 v248, v126, 24, v107
	v_cndmask_b32_e64 v119, v119, 6, s[72:73]
	v_mfma_f32_16x16x4_f32 v[236:239], v132, v32, 0
	v_sub_f32_e32 v121, v53, v115
	v_add_f32_dpp v128, v128, v128 row_ror:1 row_mask:0xf bank_mask:0xf
	v_cmp_eq_f32_e64 s[76:77], v53, v115
	global_load_dword v242, v248, s[92:93]
	v_exp_f32_e32 v165, v120
	v_add_f32_dpp v128, v128, v128 row_ror:2 row_mask:0xf bank_mask:0xf
	v_cndmask_b32_e64 v119, v119, 5, s[74:75]
	v_sub_f32_e32 v120, v49, v115
	v_add_f32_dpp v128, v128, v128 row_ror:4 row_mask:0xf bank_mask:0xf
	v_cmp_eq_f32_e64 s[72:73], v49, v115
	s_nop 0
	v_add_f32_dpp v128, v128, v128 row_ror:8 row_mask:0xf bank_mask:0xf
	v_exp_f32_e32 v164, v121
	v_rcp_f32_e32 v244, v128
	v_cndmask_b32_e64 v119, v119, 4, s[76:77]
	v_pk_mul_f32 v[134:135], v[244:245], v[134:135] op_sel_hi:[0,1]
	v_mfma_f32_16x16x4_f32 v[232:235], v133, v31, v[232:235]
	v_sub_f32_e32 v121, v45, v115
	v_cmp_eq_f32_e64 s[74:75], v45, v115
	v_pk_mul_f32 v[136:137], v[244:245], v[136:137] op_sel_hi:[0,1]
	v_exp_f32_e32 v163, v120
	global_store_dwordx4 v110, v[134:137], s[90:91] sc0 sc1
	v_cndmask_b32_e64 v119, v119, 3, s[72:73]
	v_pk_mul_f32 v[138:139], v[244:245], v[138:139] op_sel_hi:[0,1]
	v_sub_f32_e32 v120, v41, v115
	v_cmp_eq_f32_e64 s[76:77], v41, v115
	v_pk_mul_f32 v[140:141], v[244:245], v[140:141] op_sel_hi:[0,1]
	v_exp_f32_e32 v162, v121
	global_store_dwordx4 v110, v[138:141], s[90:91] offset:256 sc0 sc1
	v_cndmask_b32_e64 v119, v119, 2, s[74:75]
	v_pk_mul_f32 v[142:143], v[244:245], v[142:143] op_sel_hi:[0,1]
	v_mfma_f32_16x16x4_f32 v[236:239], v133, v33, v[236:239]
	global_load_dwordx4 v[30:33], v104, s[88:89] offset:3072
	v_sub_f32_e32 v121, v37, v115
	v_pk_mul_f32 v[144:145], v[244:245], v[144:145] op_sel_hi:[0,1]
	v_cmp_eq_f32_e64 s[72:73], v37, v115
	v_exp_f32_e32 v161, v120
	global_store_dwordx4 v110, v[142:145], s[90:91] offset:512 sc0 sc1
	v_cndmask_b32_e64 v119, v119, 1, s[76:77]
	v_pk_mul_f32 v[146:147], v[244:245], v[146:147] op_sel_hi:[0,1]
	v_exp_f32_e32 v160, v121
	v_pk_mul_f32 v[148:149], v[244:245], v[148:149] op_sel_hi:[0,1]
	v_cndmask_b32_e64 v119, v119, 0, s[72:73]
	global_store_dwordx4 v110, v[146:149], s[90:91] offset:768 sc0 sc1
	v_and_b32_e32 v123, 12, v119
	v_max3_f32 v114, v176, v180, v184
	v_and_b32_e32 v125, 3, v119
	v_add_f32_e32 v129, v160, v161
	v_add_f32_e32 v131, v162, v163
	v_max3_f32 v116, v188, v192, v196
	v_lshl_or_b32 v123, v123, 4, v125
	v_add_f32_e32 v129, v129, v164
	v_add_f32_e32 v131, v131, v165
	v_or_b32_e32 v123, v123, v102
	v_max3_f32 v114, v114, v200, v204
	v_add_f32_e32 v129, v129, v166
	v_add_f32_e32 v131, v131, v167
	v_max_u32_e32 v127, v123, v119
	v_max3_f32 v116, v116, v208, v212
	v_add_f32_e32 v129, v129, v168
	v_add_f32_e32 v131, v131, v169
	v_min_u32_dpp v127, v127, v127 row_ror:1 row_mask:0xf bank_mask:0xf
	v_add_f32_e32 v129, v129, v170
	v_max3_f32 v114, v114, v216, v220
	v_add_f32_e32 v131, v131, v171
	v_min_u32_dpp v127, v127, v127 row_ror:2 row_mask:0xf bank_mask:0xf
	v_add_f32_e32 v129, v129, v172
	v_max3_f32 v116, v116, v224, v228
	v_add_f32_e32 v131, v131, v173
	v_min_u32_dpp v127, v127, v127 row_ror:4 row_mask:0xf bank_mask:0xf
	v_add_f32_e32 v129, v129, v174
	v_add_f32_e32 v131, v131, v175
	v_max3_f32 v114, v114, v232, v236
	v_min_u32_dpp v127, v127, v127 row_ror:8 row_mask:0xf bank_mask:0xf
	v_add_f32_e32 v129, v129, v131
	v_mad_u32_u24 v249, v127, 24, v107
	s_nop 0
	v_add_f32_dpp v129, v129, v129 row_ror:1 row_mask:0xf bank_mask:0xf
	v_max_f32_e32 v114, v114, v116
	global_load_dword v243, v249, s[92:93]
	v_add_f32_dpp v129, v129, v129 row_ror:2 row_mask:0xf bank_mask:0xf
	s_nop 1
	v_add_f32_dpp v129, v129, v129 row_ror:4 row_mask:0xf bank_mask:0xf
	v_max_f32_dpp v114, v114, v114 row_ror:1 row_mask:0xf bank_mask:0xf
	s_nop 0
	v_add_f32_dpp v129, v129, v129 row_ror:8 row_mask:0xf bank_mask:0xf
	v_rcp_f32_e32 v246, v129
	s_nop 0
	v_pk_mul_f32 v[160:161], v[246:247], v[160:161] op_sel_hi:[0,1]
	v_pk_mul_f32 v[162:163], v[246:247], v[162:163] op_sel_hi:[0,1]
	v_max_f32_dpp v114, v114, v114 row_ror:2 row_mask:0xf bank_mask:0xf
	global_store_dwordx4 v111, v[160:163], s[90:91] sc0 sc1
	v_pk_mul_f32 v[164:165], v[246:247], v[164:165] op_sel_hi:[0,1]
	v_pk_mul_f32 v[166:167], v[246:247], v[166:167] op_sel_hi:[0,1]
	v_max_f32_dpp v114, v114, v114 row_ror:4 row_mask:0xf bank_mask:0xf
	global_store_dwordx4 v111, v[164:167], s[90:91] offset:256 sc0 sc1
	v_pk_mul_f32 v[168:169], v[246:247], v[168:169] op_sel_hi:[0,1]
	v_pk_mul_f32 v[170:171], v[246:247], v[170:171] op_sel_hi:[0,1]
	global_store_dwordx4 v111, v[168:171], s[90:91] offset:512 sc0 sc1
	v_max_f32_dpp v114, v114, v114 row_ror:8 row_mask:0xf bank_mask:0xf
	v_pk_mul_f32 v[172:173], v[246:247], v[172:173] op_sel_hi:[0,1]
	v_pk_mul_f32 v[174:175], v[246:247], v[174:175] op_sel_hi:[0,1]
	global_store_dwordx4 v111, v[172:175], s[90:91] offset:768 sc0 sc1
	s_add_i32 s70, s70, 1
	s_waitcnt lgkmcnt(0)
	s_lshl_b32 s84, s70, 13
	s_add_u32 s90, s80, s84
	s_addc_u32 s91, s81, 0
	s_mul_i32 s84, s70, 0xc000
	s_add_u32 s92, s94, s84
	s_addc_u32 s93, s95, 0
	s_add_i32 s84, s70, 2
	s_and_b32 s84, s84, 15
	s_lshl_b32 s82, s84, 12
	s_lshl_b32 s84, s84, 16
	s_add_u32 s84, s84, 0x787000
	s_add_u32 s86, s40, s84
	s_addc_u32 s87, s41, 0
	s_add_u32 s88, s86, 0x1000
	s_addc_u32 s89, s87, 0
	s_add_i32 s84, s70, 15
	s_and_b32 s84, s84, 15
	s_mul_i32 s84, s84, 0xc0
	s_add_u32 s83, s84, 0x10000
	v_add_u32_e32 v112, s82, v105
	v_sub_f32_e32 v120, v236, v114
	v_cmp_eq_f32_e64 s[72:73], v236, v114
	s_waitcnt vmcnt(27)
	v_mfma_f32_16x16x4_f32 v[34:37], v254, v6, 0
	ds_read2st64_b32 v[132:133], v112 offset1:1
	v_sub_f32_e32 v121, v232, v114
	v_cmp_eq_f32_e64 s[74:75], v232, v114
	v_exp_f32_e32 v149, v120
	v_cndmask_b32_e64 v118, v155, 15, s[72:73]
	v_max3_f32 v115, v177, v181, v185
	v_sub_f32_e32 v120, v228, v114
	v_cmp_eq_f32_e64 s[76:77], v228, v114
	v_exp_f32_e32 v148, v121
	v_cndmask_b32_e64 v118, v118, 14, s[74:75]
	v_mfma_f32_16x16x4_f32 v[38:41], v254, v8, 0
	v_sub_f32_e32 v121, v224, v114
	v_max3_f32 v117, v189, v193, v197
	v_cmp_eq_f32_e64 s[72:73], v224, v114
	v_exp_f32_e32 v147, v120
	v_cndmask_b32_e64 v118, v118, 13, s[76:77]
	v_sub_f32_e32 v120, v220, v114
	v_cmp_eq_f32_e64 s[74:75], v220, v114
	v_max3_f32 v115, v115, v201, v205
	v_exp_f32_e32 v146, v121
	v_cndmask_b32_e64 v118, v118, 12, s[72:73]
	v_mfma_f32_16x16x4_f32 v[34:37], v255, v7, v[34:37]
	v_sub_f32_e32 v121, v216, v114
	v_cmp_eq_f32_e64 s[76:77], v216, v114
	v_exp_f32_e32 v145, v120
	v_cndmask_b32_e64 v118, v118, 11, s[74:75]
	v_max3_f32 v117, v117, v209, v213
	v_sub_f32_e32 v120, v212, v114
	v_cmp_eq_f32_e64 s[72:73], v212, v114
	v_exp_f32_e32 v144, v121
	v_cndmask_b32_e64 v118, v118, 10, s[76:77]
	v_mfma_f32_16x16x4_f32 v[38:41], v255, v9, v[38:41]
	global_load_dwordx4 v[6:9], v104, s[86:87]
	v_sub_f32_e32 v121, v208, v114
	v_max3_f32 v115, v115, v217, v221
	v_cmp_eq_f32_e64 s[74:75], v208, v114
	v_exp_f32_e32 v143, v120
	v_cndmask_b32_e64 v118, v118, 9, s[72:73]
	v_sub_f32_e32 v120, v204, v114
	v_cmp_eq_f32_e64 s[76:77], v204, v114
	v_max3_f32 v117, v117, v225, v229
	v_exp_f32_e32 v142, v121
	v_cndmask_b32_e64 v118, v118, 8, s[74:75]
	s_waitcnt vmcnt(27)
	v_mfma_f32_16x16x4_f32 v[42:45], v254, v2, 0
	v_sub_f32_e32 v121, v200, v114
	v_cmp_eq_f32_e64 s[72:73], v200, v114
	v_exp_f32_e32 v141, v120
	v_cndmask_b32_e64 v118, v118, 7, s[76:77]
	v_max3_f32 v115, v115, v233, v237
	v_sub_f32_e32 v120, v196, v114
	v_cmp_eq_f32_e64 s[74:75], v196, v114
	v_exp_f32_e32 v140, v121
	v_cndmask_b32_e64 v118, v118, 6, s[72:73]
	v_mfma_f32_16x16x4_f32 v[46:49], v254, v4, 0
	v_sub_f32_e32 v121, v192, v114
	v_max_f32_e32 v115, v115, v117
	v_cmp_eq_f32_e64 s[76:77], v192, v114
	v_exp_f32_e32 v139, v120
	v_cndmask_b32_e64 v118, v118, 5, s[74:75]
	v_sub_f32_e32 v120, v188, v114
	v_cmp_eq_f32_e64 s[72:73], v188, v114
	v_max_f32_dpp v115, v115, v115 row_ror:1 row_mask:0xf bank_mask:0xf
	v_exp_f32_e32 v138, v121
	v_cndmask_b32_e64 v118, v118, 4, s[76:77]
	v_mfma_f32_16x16x4_f32 v[42:45], v255, v3, v[42:45]
	v_sub_f32_e32 v121, v184, v114
	v_cmp_eq_f32_e64 s[74:75], v184, v114
	v_exp_f32_e32 v137, v120
	v_cndmask_b32_e64 v118, v118, 3, s[72:73]
	v_max_f32_dpp v115, v115, v115 row_ror:2 row_mask:0xf bank_mask:0xf
	v_sub_f32_e32 v120, v180, v114
	v_cmp_eq_f32_e64 s[76:77], v180, v114
	v_exp_f32_e32 v136, v121
	v_cndmask_b32_e64 v118, v118, 2, s[74:75]
	v_mfma_f32_16x16x4_f32 v[46:49], v255, v5, v[46:49]
	global_load_dwordx4 v[2:5], v104, s[86:87] offset:1024
	v_sub_f32_e32 v121, v176, v114
	v_max_f32_dpp v115, v115, v115 row_ror:4 row_mask:0xf bank_mask:0xf
	v_cmp_eq_f32_e64 s[72:73], v176, v114
	v_exp_f32_e32 v135, v120
	v_cndmask_b32_e64 v118, v118, 1, s[76:77]
	v_exp_f32_e32 v134, v121
	v_cndmask_b32_e64 v118, v118, 0, s[72:73]
	v_max_f32_dpp v115, v115, v115 row_ror:8 row_mask:0xf bank_mask:0xf
	v_sub_f32_e32 v120, v237, v115
	v_cmp_eq_f32_e64 s[72:73], v237, v115
	v_max3_f32 v114, v178, v182, v186
	s_waitcnt vmcnt(27)
	v_mfma_f32_16x16x4_f32 v[50:53], v254, v10, 0
	v_sub_f32_e32 v121, v233, v115
	v_and_b32_e32 v122, 12, v118
	v_cmp_eq_f32_e64 s[74:75], v233, v115
	v_and_b32_e32 v124, 3, v118
	v_exp_f32_e32 v175, v120
	v_add_f32_e32 v128, v134, v135
	v_cndmask_b32_e64 v119, v155, 15, s[72:73]
	v_add_f32_e32 v130, v136, v137
	v_sub_f32_e32 v120, v229, v115
	v_max3_f32 v116, v190, v194, v198
	v_cmp_eq_f32_e64 s[76:77], v229, v115
	v_exp_f32_e32 v174, v121
	v_lshl_or_b32 v122, v122, 4, v124
	v_cndmask_b32_e64 v119, v119, 14, s[74:75]
	v_add_f32_e32 v128, v128, v138
	v_mfma_f32_16x16x4_f32 v[54:57], v254, v12, 0
	v_sub_f32_e32 v121, v225, v115
	v_add_f32_e32 v130, v130, v139
	v_cmp_eq_f32_e64 s[72:73], v225, v115
	v_or_b32_e32 v122, v122, v102
	v_exp_f32_e32 v173, v120
	v_max3_f32 v114, v114, v202, v206
	v_cndmask_b32_e64 v119, v119, 13, s[76:77]
	v_add_f32_e32 v128, v128, v140
	v_sub_f32_e32 v120, v221, v115
	v_cmp_eq_f32_e64 s[74:75], v221, v115
	v_add_f32_e32 v130, v130, v141
	v_exp_f32_e32 v172, v121
	v_max_u32_e32 v126, v122, v118
	v_cndmask_b32_e64 v119, v119, 12, s[72:73]
	v_max3_f32 v116, v116, v210, v214
	v_mfma_f32_16x16x4_f32 v[50:53], v255, v11, v[50:53]
	v_sub_f32_e32 v121, v217, v115
	v_add_f32_e32 v128, v128, v142
	v_cmp_eq_f32_e64 s[76:77], v217, v115
	v_add_f32_e32 v130, v130, v143
	v_exp_f32_e32 v171, v120
	v_min_u32_dpp v126, v126, v126 row_ror:1 row_mask:0xf bank_mask:0xf
	v_cndmask_b32_e64 v119, v119, 11, s[74:75]
	v_sub_f32_e32 v120, v213, v115
	v_add_f32_e32 v128, v128, v144
	v_cmp_eq_f32_e64 s[72:73], v213, v115
	v_max3_f32 v114, v114, v218, v222
	v_exp_f32_e32 v170, v121
	v_add_f32_e32 v130, v130, v145
	v_cndmask_b32_e64 v119, v119, 10, s[76:77]
	v_min_u32_dpp v126, v126, v126 row_ror:2 row_mask:0xf bank_mask:0xf
	v_mfma_f32_16x16x4_f32 v[54:57], v255, v13, v[54:57]
	global_load_dwordx4 v[10:13], v104, s[86:87] offset:2048
	v_sub_f32_e32 v121, v209, v115
	v_add_f32_e32 v128, v128, v146
	v_cmp_eq_f32_e64 s[74:75], v209, v115
	v_max3_f32 v116, v116, v226, v230
	v_exp_f32_e32 v169, v120
	v_cndmask_b32_e64 v119, v119, 9, s[72:73]
	v_add_f32_e32 v130, v130, v147
	v_sub_f32_e32 v120, v205, v115
	v_min_u32_dpp v126, v126, v126 row_ror:4 row_mask:0xf bank_mask:0xf
	v_cmp_eq_f32_e64 s[76:77], v205, v115
	v_add_f32_e32 v128, v128, v148
	v_exp_f32_e32 v168, v121
	v_add_f32_e32 v130, v130, v149
	v_cndmask_b32_e64 v119, v119, 8, s[74:75]
	v_max3_f32 v114, v114, v234, v238
	s_waitcnt vmcnt(24)
	v_mfma_f32_16x16x4_f32 v[58:61], v254, v14, 0
	v_sub_f32_e32 v121, v201, v115
	v_min_u32_dpp v126, v126, v126 row_ror:8 row_mask:0xf bank_mask:0xf
	v_cmp_eq_f32_e64 s[72:73], v201, v115
	v_exp_f32_e32 v167, v120
	v_add_f32_e32 v128, v128, v130
	v_cndmask_b32_e64 v119, v119, 7, s[76:77]
	v_mad_u32_u24 v248, v126, 24, v107
	v_sub_f32_e32 v120, v197, v115
	v_add_f32_dpp v128, v128, v128 row_ror:1 row_mask:0xf bank_mask:0xf
	v_cmp_eq_f32_e64 s[74:75], v197, v115
	v_max_f32_e32 v114, v114, v116
	v_exp_f32_e32 v166, v121
	global_load_dword v159, v248, s[92:93]
	v_cndmask_b32_e64 v119, v119, 6, s[72:73]
	v_add_f32_dpp v128, v128, v128 row_ror:2 row_mask:0xf bank_mask:0xf
	v_mfma_f32_16x16x4_f32 v[62:65], v254, v16, 0
	v_sub_f32_e32 v121, v193, v115
	v_cmp_eq_f32_e64 s[76:77], v193, v115
	v_add_f32_dpp v128, v128, v128 row_ror:4 row_mask:0xf bank_mask:0xf
	v_exp_f32_e32 v165, v120
	v_max_f32_dpp v114, v114, v114 row_ror:1 row_mask:0xf bank_mask:0xf
	v_cndmask_b32_e64 v119, v119, 5, s[74:75]
	v_add_f32_dpp v128, v128, v128 row_ror:8 row_mask:0xf bank_mask:0xf
	v_sub_f32_e32 v120, v189, v115
	v_rcp_f32_e32 v244, v128
	v_cmp_eq_f32_e64 s[72:73], v189, v115
	v_pk_mul_f32 v[134:135], v[244:245], v[134:135] op_sel_hi:[0,1]
	v_exp_f32_e32 v164, v121
	v_pk_mul_f32 v[136:137], v[244:245], v[136:137] op_sel_hi:[0,1]
	v_cndmask_b32_e64 v119, v119, 4, s[76:77]
	v_mfma_f32_16x16x4_f32 v[58:61], v255, v15, v[58:61]
	v_sub_f32_e32 v121, v185, v115
	v_max_f32_dpp v114, v114, v114 row_ror:2 row_mask:0xf bank_mask:0xf
	v_cmp_eq_f32_e64 s[74:75], v185, v115
	global_store_dwordx4 v108, v[134:137], s[90:91] sc0 sc1
	v_exp_f32_e32 v163, v120
	v_pk_mul_f32 v[138:139], v[244:245], v[138:139] op_sel_hi:[0,1]
	v_cndmask_b32_e64 v119, v119, 3, s[72:73]
	v_pk_mul_f32 v[140:141], v[244:245], v[140:141] op_sel_hi:[0,1]
	v_sub_f32_e32 v120, v181, v115
	v_max_f32_dpp v114, v114, v114 row_ror:4 row_mask:0xf bank_mask:0xf
	v_cmp_eq_f32_e64 s[76:77], v181, v115
	global_store_dwordx4 v108, v[138:141], s[90:91] offset:256 sc0 sc1
	v_exp_f32_e32 v162, v121
	v_cndmask_b32_e64 v119, v119, 2, s[74:75]
	v_pk_mul_f32 v[142:143], v[244:245], v[142:143] op_sel_hi:[0,1]
	v_mfma_f32_16x16x4_f32 v[62:65], v255, v17, v[62:65]
	global_load_dwordx4 v[14:17], v104, s[86:87] offset:3072
	v_sub_f32_e32 v121, v177, v115
	v_pk_mul_f32 v[144:145], v[244:245], v[144:145] op_sel_hi:[0,1]
	v_cmp_eq_f32_e64 s[72:73], v177, v115
	global_store_dwordx4 v108, v[142:145], s[90:91] offset:512 sc0 sc1
	v_exp_f32_e32 v161, v120
	v_max_f32_dpp v114, v114, v114 row_ror:8 row_mask:0xf bank_mask:0xf
	v_cndmask_b32_e64 v119, v119, 1, s[76:77]
	v_pk_mul_f32 v[146:147], v[244:245], v[146:147] op_sel_hi:[0,1]
	v_exp_f32_e32 v160, v121
	v_pk_mul_f32 v[148:149], v[244:245], v[148:149] op_sel_hi:[0,1]
	v_cndmask_b32_e64 v119, v119, 0, s[72:73]
	global_store_dwordx4 v108, v[146:149], s[90:91] offset:768 sc0 sc1
	v_sub_f32_e32 v120, v238, v114
	v_cmp_eq_f32_e64 s[72:73], v238, v114
	s_waitcnt vmcnt(13)
	s_waitcnt vmcnt(27)
	v_mfma_f32_16x16x4_f32 v[66:69], v254, v18, 0
	v_sub_f32_e32 v121, v234, v114
	v_add_u32_e32 v113, s83, v106
	v_cmp_eq_f32_e64 s[74:75], v234, v114
	ds_read2st64_b32 v[250:251], v113 offset1:12
	v_exp_f32_e32 v149, v120
	ds_read2st64_b32 v[252:253], v113 offset0:24 offset1:36
	v_cndmask_b32_e64 v118, v155, 15, s[72:73]
	v_max3_f32 v115, v179, v183, v187
	v_sub_f32_e32 v120, v230, v114
	v_and_b32_e32 v123, 12, v119
	v_cmp_eq_f32_e64 s[76:77], v230, v114
	v_and_b32_e32 v125, 3, v119
	v_exp_f32_e32 v148, v121
	v_add_f32_e32 v129, v160, v161
	v_cndmask_b32_e64 v118, v118, 14, s[74:75]
	v_add_f32_e32 v131, v162, v163
	v_mfma_f32_16x16x4_f32 v[70:73], v254, v20, 0
	v_sub_f32_e32 v121, v226, v114
	v_max3_f32 v117, v191, v195, v199
	v_cmp_eq_f32_e64 s[72:73], v226, v114
	v_lshl_or_b32 v123, v123, 4, v125
	v_exp_f32_e32 v147, v120
	v_cndmask_b32_e64 v118, v118, 13, s[76:77]
	v_add_f32_e32 v129, v129, v164
	v_sub_f32_e32 v120, v222, v114
	v_add_f32_e32 v131, v131, v165
	v_cmp_eq_f32_e64 s[74:75], v222, v114
	v_or_b32_e32 v123, v123, v102
	v_exp_f32_e32 v146, v121
	v_max3_f32 v115, v115, v203, v207
	v_cndmask_b32_e64 v118, v118, 12, s[72:73]
	v_add_f32_e32 v129, v129, v166
	v_mfma_f32_16x16x4_f32 v[66:69], v255, v19, v[66:69]
	v_sub_f32_e32 v121, v218, v114
	v_add_f32_e32 v131, v131, v167
	v_cmp_eq_f32_e64 s[76:77], v218, v114
	v_max_u32_e32 v127, v123, v119
	v_exp_f32_e32 v145, v120
	v_max3_f32 v117, v117, v211, v215
	v_cndmask_b32_e64 v118, v118, 11, s[74:75]
	v_add_f32_e32 v129, v129, v168
	v_sub_f32_e32 v120, v214, v114
	v_add_f32_e32 v131, v131, v169
	v_cmp_eq_f32_e64 s[72:73], v214, v114
	v_min_u32_dpp v127, v127, v127 row_ror:1 row_mask:0xf bank_mask:0xf
	v_exp_f32_e32 v144, v121
	v_add_f32_e32 v129, v129, v170
	v_cndmask_b32_e64 v118, v118, 10, s[76:77]
	v_mfma_f32_16x16x4_f32 v[70:73], v255, v21, v[70:73]
	global_load_dwordx4 v[18:21], v104, s[88:89]
	v_sub_f32_e32 v121, v210, v114
	v_max3_f32 v115, v115, v219, v223
	v_cmp_eq_f32_e64 s[74:75], v210, v114
	v_add_f32_e32 v131, v131, v171
	v_exp_f32_e32 v143, v120
	v_min_u32_dpp v127, v127, v127 row_ror:2 row_mask:0xf bank_mask:0xf
	v_cndmask_b32_e64 v118, v118, 9, s[72:73]
	v_add_f32_e32 v129, v129, v172
	v_sub_f32_e32 v120, v206, v114
	v_max3_f32 v117, v117, v227, v231
	v_cmp_eq_f32_e64 s[76:77], v206, v114
	v_add_f32_e32 v131, v131, v173
	v_exp_f32_e32 v142, v121
	v_min_u32_dpp v127, v127, v127 row_ror:4 row_mask:0xf bank_mask:0xf
	v_cndmask_b32_e64 v118, v118, 8, s[74:75]
	v_add_f32_e32 v129, v129, v174
	s_waitcnt vmcnt(24)
	v_mfma_f32_16x16x4_f32 v[74:77], v254, v22, 0
	v_sub_f32_e32 v121, v202, v114
	v_add_f32_e32 v131, v131, v175
	v_cmp_eq_f32_e64 s[72:73], v202, v114
	v_max3_f32 v115, v115, v235, v239
	v_exp_f32_e32 v141, v120
	v_min_u32_dpp v127, v127, v127 row_ror:8 row_mask:0xf bank_mask:0xf
	v_cndmask_b32_e64 v118, v118, 7, s[76:77]
	v_add_f32_e32 v129, v129, v131
	v_sub_f32_e32 v120, v198, v114
	v_cmp_eq_f32_e64 s[74:75], v198, v114
	v_mad_u32_u24 v249, v127, 24, v107
	v_exp_f32_e32 v140, v121
	v_add_f32_dpp v129, v129, v129 row_ror:1 row_mask:0xf bank_mask:0xf
	v_cndmask_b32_e64 v118, v118, 6, s[72:73]
	v_max_f32_e32 v115, v115, v117
	v_mfma_f32_16x16x4_f32 v[78:81], v254, v24, 0
	v_sub_f32_e32 v121, v194, v114
	global_load_dword v158, v249, s[92:93]
	v_cmp_eq_f32_e64 s[76:77], v194, v114
	v_add_f32_dpp v129, v129, v129 row_ror:2 row_mask:0xf bank_mask:0xf
	v_exp_f32_e32 v139, v120
	s_nop 0
	v_add_f32_dpp v129, v129, v129 row_ror:4 row_mask:0xf bank_mask:0xf
	v_cndmask_b32_e64 v118, v118, 5, s[74:75]
	v_max_f32_dpp v115, v115, v115 row_ror:1 row_mask:0xf bank_mask:0xf
	v_sub_f32_e32 v120, v190, v114
	v_add_f32_dpp v129, v129, v129 row_ror:8 row_mask:0xf bank_mask:0xf
	v_cmp_eq_f32_e64 s[72:73], v190, v114
	v_rcp_f32_e32 v246, v129
	v_exp_f32_e32 v138, v121
	v_pk_mul_f32 v[160:161], v[246:247], v[160:161] op_sel_hi:[0,1]
	v_cndmask_b32_e64 v118, v118, 4, s[76:77]
	v_pk_mul_f32 v[162:163], v[246:247], v[162:163] op_sel_hi:[0,1]
	v_mfma_f32_16x16x4_f32 v[74:77], v255, v23, v[74:77]
	v_sub_f32_e32 v121, v186, v114
	v_max_f32_dpp v115, v115, v115 row_ror:2 row_mask:0xf bank_mask:0xf
	v_cmp_eq_f32_e64 s[74:75], v186, v114
	v_exp_f32_e32 v137, v120
	global_store_dwordx4 v109, v[160:163], s[90:91] sc0 sc1
	v_cndmask_b32_e64 v118, v118, 3, s[72:73]
	v_pk_mul_f32 v[164:165], v[246:247], v[164:165] op_sel_hi:[0,1]
	v_sub_f32_e32 v120, v182, v114
	v_pk_mul_f32 v[166:167], v[246:247], v[166:167] op_sel_hi:[0,1]
	v_cmp_eq_f32_e64 s[76:77], v182, v114
	v_max_f32_dpp v115, v115, v115 row_ror:4 row_mask:0xf bank_mask:0xf
	v_exp_f32_e32 v136, v121
	global_store_dwordx4 v109, v[164:167], s[90:91] offset:256 sc0 sc1
	v_cndmask_b32_e64 v118, v118, 2, s[74:75]
	v_pk_mul_f32 v[168:169], v[246:247], v[168:169] op_sel_hi:[0,1]
	v_mfma_f32_16x16x4_f32 v[78:81], v255, v25, v[78:81]
	global_load_dwordx4 v[22:25], v104, s[88:89] offset:1024
	v_sub_f32_e32 v121, v178, v114
	v_pk_mul_f32 v[170:171], v[246:247], v[170:171] op_sel_hi:[0,1]
	v_cmp_eq_f32_e64 s[72:73], v178, v114
	global_store_dwordx4 v109, v[168:171], s[90:91] offset:512 sc0 sc1
	v_exp_f32_e32 v135, v120
	v_max_f32_dpp v115, v115, v115 row_ror:8 row_mask:0xf bank_mask:0xf
	v_cndmask_b32_e64 v118, v118, 1, s[76:77]
	v_pk_mul_f32 v[172:173], v[246:247], v[172:173] op_sel_hi:[0,1]
	v_exp_f32_e32 v134, v121
	v_pk_mul_f32 v[174:175], v[246:247], v[174:175] op_sel_hi:[0,1]
	v_cndmask_b32_e64 v118, v118, 0, s[72:73]
	global_store_dwordx4 v109, v[172:175], s[90:91] offset:768 sc0 sc1
	v_sub_f32_e32 v120, v239, v115
	v_cmp_eq_f32_e64 s[72:73], v239, v115
	s_waitcnt lgkmcnt(0)
	s_waitcnt vmcnt(27)
	v_mfma_f32_16x16x4_f32 v[82:85], v254, v26, 0
	v_sub_f32_e32 v121, v235, v115
	v_add_f32_e32 v250, v240, v250
	v_cmp_eq_f32_e64 s[74:75], v235, v115
	v_add_f32_e32 v251, v241, v251
	v_exp_f32_e32 v175, v120
	v_cndmask_b32_e64 v119, v155, 15, s[72:73]
	v_add_f32_e32 v252, v242, v252
	v_sub_f32_e32 v120, v231, v115
	v_add_f32_e32 v253, v243, v253
	v_cmp_eq_f32_e64 s[76:77], v231, v115
	ds_write2st64_b32 v113, v250, v251 offset1:12
	v_exp_f32_e32 v174, v121
	ds_write2st64_b32 v113, v252, v253 offset0:24 offset1:36
	v_cndmask_b32_e64 v119, v119, 14, s[74:75]
	v_mfma_f32_16x16x4_f32 v[86:89], v254, v28, 0
	v_sub_f32_e32 v121, v227, v115
	v_and_b32_e32 v122, 12, v118
	v_cmp_eq_f32_e64 s[72:73], v227, v115
	v_and_b32_e32 v124, 3, v118
	v_exp_f32_e32 v173, v120
	v_add_f32_e32 v128, v134, v135
	v_cndmask_b32_e64 v119, v119, 13, s[76:77]
	v_sub_f32_e32 v120, v223, v115
	v_add_f32_e32 v130, v136, v137
	v_cmp_eq_f32_e64 s[74:75], v223, v115
	v_lshl_or_b32 v122, v122, 4, v124
	v_exp_f32_e32 v172, v121
	v_add_f32_e32 v128, v128, v138
	v_cndmask_b32_e64 v119, v119, 12, s[72:73]
	v_add_f32_e32 v130, v130, v139
	v_mfma_f32_16x16x4_f32 v[82:85], v255, v27, v[82:85]
	v_sub_f32_e32 v121, v219, v115
	v_cmp_eq_f32_e64 s[76:77], v219, v115
	v_or_b32_e32 v122, v122, v102
	v_exp_f32_e32 v171, v120
	v_add_f32_e32 v128, v128, v140
	v_cndmask_b32_e64 v119, v119, 11, s[74:75]
	v_add_f32_e32 v130, v130, v141
	v_sub_f32_e32 v120, v215, v115
	v_cmp_eq_f32_e64 s[72:73], v215, v115
	v_max_u32_e32 v126, v122, v118
	v_exp_f32_e32 v170, v121
	v_add_f32_e32 v128, v128, v142
	v_cndmask_b32_e64 v119, v119, 10, s[76:77]
	v_add_f32_e32 v130, v130, v143
	v_mfma_f32_16x16x4_f32 v[86:89], v255, v29, v[86:89]
	global_load_dwordx4 v[26:29], v104, s[88:89] offset:2048
	v_sub_f32_e32 v121, v211, v115
	v_min_u32_dpp v126, v126, v126 row_ror:1 row_mask:0xf bank_mask:0xf
	v_cmp_eq_f32_e64 s[74:75], v211, v115
	v_exp_f32_e32 v169, v120
	v_add_f32_e32 v128, v128, v144
	v_cndmask_b32_e64 v119, v119, 9, s[72:73]
	v_add_f32_e32 v130, v130, v145
	v_sub_f32_e32 v120, v207, v115
	v_min_u32_dpp v126, v126, v126 row_ror:2 row_mask:0xf bank_mask:0xf
	v_cmp_eq_f32_e64 s[76:77], v207, v115
	v_add_f32_e32 v128, v128, v146
	v_exp_f32_e32 v168, v121
	v_cndmask_b32_e64 v119, v119, 8, s[74:75]
	v_add_f32_e32 v130, v130, v147
	s_waitcnt vmcnt(24)
	v_mfma_f32_16x16x4_f32 v[90:93], v254, v30, 0
	v_sub_f32_e32 v121, v203, v115
	v_min_u32_dpp v126, v126, v126 row_ror:4 row_mask:0xf bank_mask:0xf
	v_cmp_eq_f32_e64 s[72:73], v203, v115
	v_add_f32_e32 v128, v128, v148
	v_exp_f32_e32 v167, v120
	v_cndmask_b32_e64 v119, v119, 7, s[76:77]
	v_add_f32_e32 v130, v130, v149
	v_sub_f32_e32 v120, v199, v115
	v_min_u32_dpp v126, v126, v126 row_ror:8 row_mask:0xf bank_mask:0xf
	v_cmp_eq_f32_e64 s[74:75], v199, v115
	v_add_f32_e32 v128, v128, v130
	v_exp_f32_e32 v166, v121
	v_mad_u32_u24 v248, v126, 24, v107
	v_cndmask_b32_e64 v119, v119, 6, s[72:73]
	v_mfma_f32_16x16x4_f32 v[94:97], v254, v32, 0
	v_sub_f32_e32 v121, v195, v115
	v_add_f32_dpp v128, v128, v128 row_ror:1 row_mask:0xf bank_mask:0xf
	v_cmp_eq_f32_e64 s[76:77], v195, v115
	global_load_dword v157, v248, s[92:93]
	v_exp_f32_e32 v165, v120
	v_add_f32_dpp v128, v128, v128 row_ror:2 row_mask:0xf bank_mask:0xf
	v_cndmask_b32_e64 v119, v119, 5, s[74:75]
	v_sub_f32_e32 v120, v191, v115
	v_add_f32_dpp v128, v128, v128 row_ror:4 row_mask:0xf bank_mask:0xf
	v_cmp_eq_f32_e64 s[72:73], v191, v115
	s_nop 0
	v_add_f32_dpp v128, v128, v128 row_ror:8 row_mask:0xf bank_mask:0xf
	v_exp_f32_e32 v164, v121
	v_rcp_f32_e32 v244, v128
	v_cndmask_b32_e64 v119, v119, 4, s[76:77]
	v_pk_mul_f32 v[134:135], v[244:245], v[134:135] op_sel_hi:[0,1]
	v_mfma_f32_16x16x4_f32 v[90:93], v255, v31, v[90:93]
	v_sub_f32_e32 v121, v187, v115
	v_cmp_eq_f32_e64 s[74:75], v187, v115
	v_pk_mul_f32 v[136:137], v[244:245], v[136:137] op_sel_hi:[0,1]
	v_exp_f32_e32 v163, v120
	global_store_dwordx4 v110, v[134:137], s[90:91] sc0 sc1
	v_cndmask_b32_e64 v119, v119, 3, s[72:73]
	v_pk_mul_f32 v[138:139], v[244:245], v[138:139] op_sel_hi:[0,1]
	v_sub_f32_e32 v120, v183, v115
	v_cmp_eq_f32_e64 s[76:77], v183, v115
	v_pk_mul_f32 v[140:141], v[244:245], v[140:141] op_sel_hi:[0,1]
	v_exp_f32_e32 v162, v121
	global_store_dwordx4 v110, v[138:141], s[90:91] offset:256 sc0 sc1
	v_cndmask_b32_e64 v119, v119, 2, s[74:75]
	v_pk_mul_f32 v[142:143], v[244:245], v[142:143] op_sel_hi:[0,1]
	v_mfma_f32_16x16x4_f32 v[94:97], v255, v33, v[94:97]
	global_load_dwordx4 v[30:33], v104, s[88:89] offset:3072
	v_sub_f32_e32 v121, v179, v115
	v_pk_mul_f32 v[144:145], v[244:245], v[144:145] op_sel_hi:[0,1]
	v_cmp_eq_f32_e64 s[72:73], v179, v115
	v_exp_f32_e32 v161, v120
	global_store_dwordx4 v110, v[142:145], s[90:91] offset:512 sc0 sc1
	v_cndmask_b32_e64 v119, v119, 1, s[76:77]
	v_pk_mul_f32 v[146:147], v[244:245], v[146:147] op_sel_hi:[0,1]
	v_exp_f32_e32 v160, v121
	v_pk_mul_f32 v[148:149], v[244:245], v[148:149] op_sel_hi:[0,1]
	v_cndmask_b32_e64 v119, v119, 0, s[72:73]
	global_store_dwordx4 v110, v[146:149], s[90:91] offset:768 sc0 sc1
	v_and_b32_e32 v123, 12, v119
	v_max3_f32 v114, v34, v38, v42
	v_and_b32_e32 v125, 3, v119
	v_add_f32_e32 v129, v160, v161
	v_add_f32_e32 v131, v162, v163
	v_max3_f32 v116, v46, v50, v54
	v_lshl_or_b32 v123, v123, 4, v125
	v_add_f32_e32 v129, v129, v164
	v_add_f32_e32 v131, v131, v165
	v_or_b32_e32 v123, v123, v102
	v_max3_f32 v114, v114, v58, v62
	v_add_f32_e32 v129, v129, v166
	v_add_f32_e32 v131, v131, v167
	v_max_u32_e32 v127, v123, v119
	v_max3_f32 v116, v116, v66, v70
	v_add_f32_e32 v129, v129, v168
	v_add_f32_e32 v131, v131, v169
	v_min_u32_dpp v127, v127, v127 row_ror:1 row_mask:0xf bank_mask:0xf
	v_add_f32_e32 v129, v129, v170
	v_max3_f32 v114, v114, v74, v78
	v_add_f32_e32 v131, v131, v171
	v_min_u32_dpp v127, v127, v127 row_ror:2 row_mask:0xf bank_mask:0xf
	v_add_f32_e32 v129, v129, v172
	v_max3_f32 v116, v116, v82, v86
	v_add_f32_e32 v131, v131, v173
	v_min_u32_dpp v127, v127, v127 row_ror:4 row_mask:0xf bank_mask:0xf
	v_add_f32_e32 v129, v129, v174
	v_add_f32_e32 v131, v131, v175
	v_max3_f32 v114, v114, v90, v94
	v_min_u32_dpp v127, v127, v127 row_ror:8 row_mask:0xf bank_mask:0xf
	v_add_f32_e32 v129, v129, v131
	v_mad_u32_u24 v249, v127, 24, v107
	s_nop 0
	v_add_f32_dpp v129, v129, v129 row_ror:1 row_mask:0xf bank_mask:0xf
	v_max_f32_e32 v114, v114, v116
	global_load_dword v156, v249, s[92:93]
	v_add_f32_dpp v129, v129, v129 row_ror:2 row_mask:0xf bank_mask:0xf
	s_nop 1
	v_add_f32_dpp v129, v129, v129 row_ror:4 row_mask:0xf bank_mask:0xf
	v_max_f32_dpp v114, v114, v114 row_ror:1 row_mask:0xf bank_mask:0xf
	s_nop 0
	v_add_f32_dpp v129, v129, v129 row_ror:8 row_mask:0xf bank_mask:0xf
	v_rcp_f32_e32 v246, v129
	s_nop 0
	v_pk_mul_f32 v[160:161], v[246:247], v[160:161] op_sel_hi:[0,1]
	v_pk_mul_f32 v[162:163], v[246:247], v[162:163] op_sel_hi:[0,1]
	v_max_f32_dpp v114, v114, v114 row_ror:2 row_mask:0xf bank_mask:0xf
	global_store_dwordx4 v111, v[160:163], s[90:91] sc0 sc1
	v_pk_mul_f32 v[164:165], v[246:247], v[164:165] op_sel_hi:[0,1]
	v_pk_mul_f32 v[166:167], v[246:247], v[166:167] op_sel_hi:[0,1]
	v_max_f32_dpp v114, v114, v114 row_ror:4 row_mask:0xf bank_mask:0xf
	global_store_dwordx4 v111, v[164:167], s[90:91] offset:256 sc0 sc1
	v_pk_mul_f32 v[168:169], v[246:247], v[168:169] op_sel_hi:[0,1]
	v_pk_mul_f32 v[170:171], v[246:247], v[170:171] op_sel_hi:[0,1]
	global_store_dwordx4 v111, v[168:171], s[90:91] offset:512 sc0 sc1
	v_max_f32_dpp v114, v114, v114 row_ror:8 row_mask:0xf bank_mask:0xf
	v_pk_mul_f32 v[172:173], v[246:247], v[172:173] op_sel_hi:[0,1]
	v_pk_mul_f32 v[174:175], v[246:247], v[174:175] op_sel_hi:[0,1]
	global_store_dwordx4 v111, v[172:175], s[90:91] offset:768 sc0 sc1
	s_add_i32 s70, s70, 1
	s_cmp_lt_u32 s70, 16
	s_cbranch_scc1 .Lk3m_loop
.LBB2_422:
	s_and_saveexec_b64 s[4:5], s[0:1]
	s_cbranch_execz .LBB2_424
	s_waitcnt vmcnt(22)
	v_mad_u32_u24 v2, v150, 24, v152
	s_mov_b32 s0, 0x10000
	v_add3_u32 v2, v2, v102, s0
	v_add_u32_e32 v6, 64, v2
	ds_read2st64_b32 v[2:3], v6 offset0:11 offset1:23
	ds_read2st64_b32 v[4:5], v6 offset0:35 offset1:47
	s_waitcnt vmcnt(4) lgkmcnt(1)
	v_add_f32_e32 v2, v159, v2
	s_waitcnt vmcnt(4)
	v_add_f32_e32 v3, v158, v3
	s_waitcnt vmcnt(4) lgkmcnt(0)
	v_add_f32_e32 v4, v157, v4
	ds_write2st64_b32 v6, v2, v3 offset0:11 offset1:23
	s_waitcnt vmcnt(4)
	v_add_f32_e32 v2, v156, v5
	ds_write2st64_b32 v6, v4, v2 offset0:35 offset1:47
.LBB2_424:
	s_or_b64 exec, exec, s[4:5]
	s_movk_i32 s0, 0x300
	s_waitcnt vmcnt(22)
	v_mov_b32_e32 v2, 0x10000
	v_cmp_gt_u32_e32 vcc, s0, v0
	v_lshl_or_b32 v2, v0, 2, v2
	s_waitcnt vmcnt(4)
	v_mov_b32_e32 v32, 0
	v_mov_b32_e32 v35, 0
	s_waitcnt lgkmcnt(0)
	s_barrier
	s_and_saveexec_b64 s[0:1], vcc
	ds_read_b32 v35, v2
	s_or_b64 exec, exec, s[0:1]
	s_and_saveexec_b64 s[0:1], vcc
	ds_read_b32 v32, v2 offset:3072
	s_or_b64 exec, exec, s[0:1]
	v_mov_b32_e32 v31, 0
	v_mov_b32_e32 v34, 0
	s_and_saveexec_b64 s[0:1], vcc
	ds_read_b32 v34, v2 offset:6144
	s_or_b64 exec, exec, s[0:1]
	s_and_saveexec_b64 s[0:1], vcc
	ds_read_b32 v31, v2 offset:9216
	s_or_b64 exec, exec, s[0:1]
	v_mov_b32_e32 v29, 0
	v_mov_b32_e32 v33, 0
	s_and_saveexec_b64 s[0:1], vcc
	ds_read_b32 v33, v2 offset:12288
	s_or_b64 exec, exec, s[0:1]
	s_and_saveexec_b64 s[0:1], vcc
	ds_read_b32 v29, v2 offset:15360
	s_or_b64 exec, exec, s[0:1]
	v_mov_b32_e32 v28, 0
	v_mov_b32_e32 v30, 0
	s_and_saveexec_b64 s[0:1], vcc
	ds_read_b32 v30, v2 offset:18432
	s_or_b64 exec, exec, s[0:1]
	s_and_saveexec_b64 s[0:1], vcc
	ds_read_b32 v28, v2 offset:21504
	s_or_b64 exec, exec, s[0:1]
	v_mov_b32_e32 v24, 0
	v_mov_b32_e32 v27, 0
	s_and_saveexec_b64 s[0:1], vcc
	ds_read_b32 v27, v2 offset:24576
	s_or_b64 exec, exec, s[0:1]
	s_and_saveexec_b64 s[0:1], vcc
	ds_read_b32 v24, v2 offset:27648
	s_or_b64 exec, exec, s[0:1]
	v_mov_b32_e32 v23, 0
	v_mov_b32_e32 v26, 0
	s_and_saveexec_b64 s[0:1], vcc
	ds_read_b32 v26, v2 offset:30720
	s_or_b64 exec, exec, s[0:1]
	s_and_saveexec_b64 s[0:1], vcc
	ds_read_b32 v23, v2 offset:33792
	s_or_b64 exec, exec, s[0:1]
	v_mov_b32_e32 v21, 0
	v_mov_b32_e32 v25, 0
	s_and_saveexec_b64 s[0:1], vcc
	ds_read_b32 v25, v2 offset:36864
	s_or_b64 exec, exec, s[0:1]
	s_and_saveexec_b64 s[0:1], vcc
	ds_read_b32 v21, v2 offset:39936
	s_or_b64 exec, exec, s[0:1]
	v_mov_b32_e32 v20, 0
	v_mov_b32_e32 v22, 0
	s_and_saveexec_b64 s[0:1], vcc
	ds_read_b32 v22, v2 offset:43008
	s_or_b64 exec, exec, s[0:1]
	s_and_saveexec_b64 s[0:1], vcc
	ds_read_b32 v20, v2 offset:46080
	s_or_b64 exec, exec, s[0:1]
	s_movk_i32 s0, 0x100
	v_cmp_gt_u32_e64 s[0:1], s0, v0
	v_mov_b32_e32 v16, 0
	v_mov_b32_e32 v19, 0
	s_and_saveexec_b64 s[4:5], s[0:1]
	ds_read_b32 v19, v2 offset:2048
	s_or_b64 exec, exec, s[4:5]
	s_and_saveexec_b64 s[4:5], s[0:1]
	ds_read_b32 v16, v2 offset:5120
	s_or_b64 exec, exec, s[4:5]
	v_mov_b32_e32 v15, 0
	v_mov_b32_e32 v18, 0
	s_and_saveexec_b64 s[4:5], s[0:1]
	ds_read_b32 v18, v2 offset:8192
	s_or_b64 exec, exec, s[4:5]
	s_and_saveexec_b64 s[4:5], s[0:1]
	ds_read_b32 v15, v2 offset:11264
	s_or_b64 exec, exec, s[4:5]
	v_mov_b32_e32 v13, 0
	v_mov_b32_e32 v17, 0
	s_and_saveexec_b64 s[4:5], s[0:1]
	ds_read_b32 v17, v2 offset:14336
	s_or_b64 exec, exec, s[4:5]
	s_and_saveexec_b64 s[4:5], s[0:1]
	ds_read_b32 v13, v2 offset:17408
	s_or_b64 exec, exec, s[4:5]
	v_mov_b32_e32 v12, 0
	v_mov_b32_e32 v14, 0
	s_and_saveexec_b64 s[4:5], s[0:1]
	ds_read_b32 v14, v2 offset:20480
	s_or_b64 exec, exec, s[4:5]
	s_and_saveexec_b64 s[4:5], s[0:1]
	ds_read_b32 v12, v2 offset:23552
	s_or_b64 exec, exec, s[4:5]
	v_mov_b32_e32 v8, 0
	v_mov_b32_e32 v11, 0
	s_and_saveexec_b64 s[4:5], s[0:1]
	ds_read_b32 v11, v2 offset:26624
	s_or_b64 exec, exec, s[4:5]
	s_and_saveexec_b64 s[4:5], s[0:1]
	ds_read_b32 v8, v2 offset:29696
	s_or_b64 exec, exec, s[4:5]
	v_mov_b32_e32 v7, 0
	v_mov_b32_e32 v10, 0
	s_and_saveexec_b64 s[4:5], s[0:1]
	ds_read_b32 v10, v2 offset:32768
	s_or_b64 exec, exec, s[4:5]
	s_and_saveexec_b64 s[4:5], s[0:1]
	ds_read_b32 v7, v2 offset:35840
	s_or_b64 exec, exec, s[4:5]
	v_mov_b32_e32 v5, 0
	v_mov_b32_e32 v9, 0
	s_and_saveexec_b64 s[4:5], s[0:1]
	ds_read_b32 v9, v2 offset:38912
	s_or_b64 exec, exec, s[4:5]
	s_and_saveexec_b64 s[4:5], s[0:1]
	ds_read_b32 v5, v2 offset:41984
	s_or_b64 exec, exec, s[4:5]
	v_mov_b32_e32 v4, 0
	v_mov_b32_e32 v6, 0
	s_and_saveexec_b64 s[4:5], s[0:1]
	ds_read_b32 v6, v2 offset:45056
	s_or_b64 exec, exec, s[4:5]
	s_and_saveexec_b64 s[4:5], s[0:1]
	ds_read_b32 v4, v2 offset:48128
	s_or_b64 exec, exec, s[4:5]
	s_waitcnt lgkmcnt(0)
	v_mul_f32_e32 v2, v19, v19
	v_fmac_f32_e32 v2, v35, v35
	s_nop 1
	v_add_f32_dpp v2, v2, v2 row_ror:1 row_mask:0xf bank_mask:0xf bound_ctrl:1
	s_nop 1
	v_add_f32_dpp v2, v2, v2 row_ror:2 row_mask:0xf bank_mask:0xf bound_ctrl:1
	s_nop 1
	v_add_f32_dpp v2, v2, v2 row_ror:4 row_mask:0xf bank_mask:0xf bound_ctrl:1
	s_nop 1
	v_add_f32_dpp v2, v2, v2 row_ror:8 row_mask:0xf bank_mask:0xf bound_ctrl:1
	ds_bpermute_b32 v3, v1, v2
	s_waitcnt lgkmcnt(0)
	v_add_f32_e32 v3, v2, v3
	ds_bpermute_b32 v36, v151, v3
	v_mov_b32_e32 v2, 0x1c800
	v_lshl_or_b32 v2, v150, 6, v2
	s_and_saveexec_b64 s[4:5], s[2:3]
	s_cbranch_execz .LBB2_490
	s_waitcnt lgkmcnt(0)
	v_add_f32_e32 v3, v3, v36
	ds_write_b32 v2, v3

	.amdhsa_kernel _Z7k3_mainPKhPKfS2_S2_S2_PfS3_S3_
		.amdhsa_group_segment_fixed_size 117312
		.amdhsa_private_segment_fixed_size 0
		.amdhsa_kernarg_size 64
		.amdhsa_user_sgpr_count 2
		.amdhsa_user_sgpr_dispatch_ptr 0
		.amdhsa_user_sgpr_queue_ptr 0
		.amdhsa_user_sgpr_kernarg_segment_ptr 1
		.amdhsa_user_sgpr_dispatch_id 0
		.amdhsa_user_sgpr_kernarg_preload_length 0
		.amdhsa_user_sgpr_kernarg_preload_offset 0
		.amdhsa_user_sgpr_private_segment_size 0
		.amdhsa_uses_dynamic_stack 0
		.amdhsa_enable_private_segment 0
		.amdhsa_system_sgpr_workgroup_id_x 1
		.amdhsa_system_sgpr_workgroup_id_y 0
		.amdhsa_system_sgpr_workgroup_id_z 0
		.amdhsa_system_sgpr_workgroup_info 0
		.amdhsa_system_vgpr_workitem_id 0
		.amdhsa_next_free_vgpr 256
		.amdhsa_next_free_sgpr 96
		.amdhsa_accum_offset 256
		.amdhsa_reserve_vcc 1
		.amdhsa_float_round_mode_32 0
		.amdhsa_float_round_mode_16_64 0
		.amdhsa_float_denorm_mode_32 3
		.amdhsa_float_denorm_mode_16_64 3
		.amdhsa_dx10_clamp 1
		.amdhsa_ieee_mode 1
		.amdhsa_fp16_overflow 0
		.amdhsa_tg_split 0
		.amdhsa_exception_fp_ieee_invalid_op 0
		.amdhsa_exception_fp_denorm_src 0
		.amdhsa_exception_fp_ieee_div_zero 0
		.amdhsa_exception_fp_ieee_overflow 0
		.amdhsa_exception_fp_ieee_underflow 0
		.amdhsa_exception_fp_ieee_inexact 0
		.amdhsa_exception_int_div_zero 0
	.end_amdhsa_kernel

amdhsa.kernels:
  - .agpr_count:     0
    .args:
      - .actual_access:  read_only
        .address_space:  global
        .offset:         0
        .size:           8
        .value_kind:     global_buffer
      - .actual_access:  read_only
        .address_space:  global
        .offset:         8
        .size:           8
        .value_kind:     global_buffer
      - .actual_access:  read_only
        .address_space:  global
        .offset:         16
        .size:           8
        .value_kind:     global_buffer
      - .actual_access:  write_only
        .address_space:  global
        .offset:         24
        .size:           8
        .value_kind:     global_buffer
    .group_segment_fixed_size: 0
    .kernarg_segment_align: 8
    .kernarg_segment_size: 32
    .language:       OpenCL C
    .language_version:
      - 2
      - 0
    .max_flat_workgroup_size: 256
    .name:           _Z7k0_prepPKfS0_S0_Ph
    .private_segment_fixed_size: 0
    .sgpr_count:     24
    .sgpr_spill_count: 0
    .symbol:         _Z7k0_prepPKfS0_S0_Ph.kd
    .uniform_work_group_size: 1
    .uses_dynamic_stack: false
    .vgpr_count:     31
    .vgpr_spill_count: 0
    .wavefront_size: 64
  - .agpr_count:     76
    .args:
      - .actual_access:  read_only
        .address_space:  global
        .offset:         0
        .size:           8
        .value_kind:     global_buffer
      - .actual_access:  write_only
        .address_space:  global
        .offset:         8
        .size:           8
        .value_kind:     global_buffer
    .group_segment_fixed_size: 73728
    .kernarg_segment_align: 8
    .kernarg_segment_size: 16
    .language:       OpenCL C
    .language_version:
      - 2
      - 0
    .max_flat_workgroup_size: 256
    .name:           _Z7k1_gemmPKhPf
    .private_segment_fixed_size: 0
    .sgpr_count:     18
    .sgpr_spill_count: 0
    .symbol:         _Z7k1_gemmPKhPf.kd
    .uniform_work_group_size: 1
    .uses_dynamic_stack: false
    .vgpr_count:     332
    .vgpr_spill_count: 0
    .wavefront_size: 64
  - .agpr_count:     0
    .args:
      - .actual_access:  read_only
        .address_space:  global
        .offset:         0
        .size:           8
        .value_kind:     global_buffer
      - .actual_access:  read_only
        .address_space:  global
        .offset:         8
        .size:           8
        .value_kind:     global_buffer
      - .actual_access:  read_only
        .address_space:  global
        .offset:         16
        .size:           8
        .value_kind:     global_buffer
      - .actual_access:  read_only
        .address_space:  global
        .offset:         24
        .size:           8
        .value_kind:     global_buffer
      - .actual_access:  read_only
        .address_space:  global
        .offset:         32
        .size:           8
        .value_kind:     global_buffer
      - .actual_access:  write_only
        .address_space:  global
        .offset:         40
        .size:           8
        .value_kind:     global_buffer
      - .actual_access:  write_only
        .address_space:  global
        .offset:         48
        .size:           8
        .value_kind:     global_buffer
      - .actual_access:  write_only
        .address_space:  global
        .offset:         56
        .size:           8
        .value_kind:     global_buffer
    .group_segment_fixed_size: 117312
    .kernarg_segment_align: 8
    .kernarg_segment_size: 64
    .language:       OpenCL C
    .language_version:
      - 2
      - 0
    .max_flat_workgroup_size: 512
    .name:           _Z7k3_mainPKhPKfS2_S2_S2_PfS3_S3_
    .private_segment_fixed_size: 0
    .sgpr_count:     64
    .sgpr_spill_count: 0
    .symbol:         _Z7k3_mainPKhPKfS2_S2_S2_PfS3_S3_.kd
    .uniform_work_group_size: 1
    .uses_dynamic_stack: false
    .vgpr_count:     256
    .vgpr_spill_count: 0
    .wavefront_size: 64
